# in-projection epilogue: erf-gelu blocks regenerated with interleaved pair chains (no hazard nops), sign select via v_bfi
# speedup vs baseline: 1.0093x; 1.0055x over previous
.LBB0_249:
	v_readlane_b32 s0, v254, 13
	v_readlane_b32 s1, v254, 14
	v_mbcnt_lo_u32_b32 v165, -1, 0
	v_mbcnt_hi_u32_b32 v165, -1, v165
	s_mov_b64 s[6:7], s[100:101]
	s_cmp_lt_i32 s83, 8
	s_cselect_b64 s[0:1], -1, 0
	s_cmp_gt_i32 s83, 7
	v_mov_b32_e32 v180, v96
	v_mov_b32_e32 v181, v97
	v_mov_b32_e32 v182, v98
	v_mov_b32_e32 v183, v99
	v_mov_b32_e32 v167, v100
	v_mov_b32_e32 v169, v101
	v_mov_b32_e32 v171, v102
	v_mov_b32_e32 v179, v103
	s_cbranch_scc1 .LBB0_251
	v_mov_b32_e32 v238, s60
	v_and_b32_e32 v214, 0x7fffffff, v96
	v_and_b32_e32 v215, 0x7fffffff, v97
	v_and_b32_e32 v220, 0x7fffffff, v98
	v_and_b32_e32 v221, 0x7fffffff, v99
	v_and_b32_e32 v226, 0x7fffffff, v100
	v_and_b32_e32 v227, 0x7fffffff, v101
	v_and_b32_e32 v232, 0x7fffffff, v102
	v_and_b32_e32 v233, 0x7fffffff, v103
	v_pk_fma_f32 v[214:215], v[214:215], s[56:57], 1.0 op_sel_hi:[1,0,0]
	v_pk_fma_f32 v[220:221], v[220:221], s[56:57], 1.0 op_sel_hi:[1,0,0]
	v_pk_fma_f32 v[226:227], v[226:227], s[56:57], 1.0 op_sel_hi:[1,0,0]
	v_pk_fma_f32 v[232:233], v[232:233], s[56:57], 1.0 op_sel_hi:[1,0,0]
	v_pk_mul_f32 v[218:219], v[96:97], v[96:97]
	v_pk_mul_f32 v[224:225], v[98:99], v[98:99]
	v_pk_mul_f32 v[230:231], v[100:101], v[100:101]
	v_pk_mul_f32 v[236:237], v[102:103], v[102:103]
	v_rcp_f32_e32 v214, v214
	v_rcp_f32_e32 v215, v215
	v_rcp_f32_e32 v220, v220
	v_rcp_f32_e32 v221, v221
	v_rcp_f32_e32 v226, v226
	v_rcp_f32_e32 v227, v227
	v_rcp_f32_e32 v232, v232
	v_rcp_f32_e32 v233, v233
	v_pk_mul_f32 v[218:219], v[218:219], s[68:69] op_sel_hi:[1,0]
	v_pk_mul_f32 v[224:225], v[224:225], s[68:69] op_sel_hi:[1,0]
	v_pk_mul_f32 v[230:231], v[230:231], s[68:69] op_sel_hi:[1,0]
	v_pk_mul_f32 v[236:237], v[236:237], s[68:69] op_sel_hi:[1,0]
	v_pk_fma_f32 v[216:217], v[214:215], s[58:59], v[238:239] op_sel_hi:[1,0,0]
	v_pk_fma_f32 v[222:223], v[220:221], s[58:59], v[238:239] op_sel_hi:[1,0,0]
	v_pk_fma_f32 v[228:229], v[226:227], s[58:59], v[238:239] op_sel_hi:[1,0,0]
	v_pk_fma_f32 v[234:235], v[232:233], s[58:59], v[238:239] op_sel_hi:[1,0,0]
	v_exp_f32_e32 v218, v218
	v_exp_f32_e32 v219, v219
	v_exp_f32_e32 v224, v224
	v_exp_f32_e32 v225, v225
	v_exp_f32_e32 v230, v230
	v_exp_f32_e32 v231, v231
	v_exp_f32_e32 v236, v236
	v_exp_f32_e32 v237, v237
	v_pk_fma_f32 v[216:217], v[214:215], v[216:217], s[62:63] op_sel_hi:[1,1,0]
	v_pk_fma_f32 v[222:223], v[220:221], v[222:223], s[62:63] op_sel_hi:[1,1,0]
	v_pk_fma_f32 v[228:229], v[226:227], v[228:229], s[62:63] op_sel_hi:[1,1,0]
	v_pk_fma_f32 v[234:235], v[232:233], v[234:235], s[62:63] op_sel_hi:[1,1,0]
	v_pk_fma_f32 v[216:217], v[214:215], v[216:217], s[64:65] op_sel_hi:[1,1,0]
	v_pk_fma_f32 v[222:223], v[220:221], v[222:223], s[64:65] op_sel_hi:[1,1,0]
	v_pk_fma_f32 v[228:229], v[226:227], v[228:229], s[64:65] op_sel_hi:[1,1,0]
	v_pk_fma_f32 v[234:235], v[232:233], v[234:235], s[64:65] op_sel_hi:[1,1,0]
	v_pk_fma_f32 v[216:217], v[214:215], v[216:217], s[66:67] op_sel_hi:[1,1,0]
	v_pk_fma_f32 v[222:223], v[220:221], v[222:223], s[66:67] op_sel_hi:[1,1,0]
	v_pk_fma_f32 v[228:229], v[226:227], v[228:229], s[66:67] op_sel_hi:[1,1,0]
	v_pk_fma_f32 v[234:235], v[232:233], v[234:235], s[66:67] op_sel_hi:[1,1,0]
	v_pk_mul_f32 v[216:217], v[214:215], v[216:217]
	v_pk_mul_f32 v[222:223], v[220:221], v[222:223]
	v_pk_mul_f32 v[228:229], v[226:227], v[228:229]
	v_pk_mul_f32 v[234:235], v[232:233], v[234:235]
	v_pk_mul_f32 v[216:217], v[218:219], v[216:217]
	v_pk_mul_f32 v[222:223], v[224:225], v[222:223]
	v_pk_mul_f32 v[228:229], v[230:231], v[228:229]
	v_pk_mul_f32 v[234:235], v[236:237], v[234:235]
	v_pk_mul_f32 v[214:215], v[96:97], v[216:217]
	v_pk_mul_f32 v[220:221], v[98:99], v[222:223]
	v_pk_mul_f32 v[226:227], v[100:101], v[228:229]
	v_pk_mul_f32 v[232:233], v[102:103], v[234:235]
	v_pk_fma_f32 v[218:219], v[96:97], v[216:217], v[96:97] neg_lo:[1,0,0] neg_hi:[1,0,0]
	v_pk_fma_f32 v[224:225], v[98:99], v[222:223], v[98:99] neg_lo:[1,0,0] neg_hi:[1,0,0]
	v_pk_fma_f32 v[230:231], v[100:101], v[228:229], v[100:101] neg_lo:[1,0,0] neg_hi:[1,0,0]
	v_pk_fma_f32 v[236:237], v[102:103], v[234:235], v[102:103] neg_lo:[1,0,0] neg_hi:[1,0,0]
	v_ashrrev_i32_e32 v216, 31, v96
	v_ashrrev_i32_e32 v217, 31, v97
	v_ashrrev_i32_e32 v222, 31, v98
	v_ashrrev_i32_e32 v223, 31, v99
	v_ashrrev_i32_e32 v228, 31, v100
	v_ashrrev_i32_e32 v229, 31, v101
	v_ashrrev_i32_e32 v234, 31, v102
	v_ashrrev_i32_e32 v235, 31, v103
	v_bfi_b32 v180, v216, v214, v218
	v_bfi_b32 v181, v217, v215, v219
	v_bfi_b32 v182, v222, v220, v224
	v_bfi_b32 v183, v223, v221, v225
	v_bfi_b32 v167, v228, v226, v230
	v_bfi_b32 v169, v229, v227, v231
	v_bfi_b32 v171, v234, v232, v236
	v_bfi_b32 v179, v235, v233, v237
.LBB0_251:
	s_lshl_b32 s25, s43, 8
	s_add_i32 s25, s25, s63
	v_and_or_b32 v163, v165, 15, s25
	s_lshl_b32 s25, s83, 8
	s_or_b32 s25, s25, s84
	v_and_b32_e32 v165, -16, v165
	v_add_u32_e32 v172, s25, v165
	v_ashrrev_i32_e32 v173, 31, v172
	s_waitcnt lgkmcnt(0)
	v_lshl_add_u64 v[172:173], v[172:173], 1, s[6:7]
	s_mov_b64 s[6:7], 0x3a000000
	v_lshl_add_u64 v[172:173], v[172:173], 0, s[6:7]
	v_mad_i64_i32 v[174:175], s[6:7], v163, s94, v[172:173]
	v_cndmask_b32_e64 v165, 0, 1, s[0:1]
	v_cvt_pk_bf16_f32 v184, v167, v169
	v_cvt_pk_bf16_f32 v185, v171, v179
	v_cvt_pk_bf16_f32 v186, v180, v181
	v_cvt_pk_bf16_f32 v187, v182, v183
	v_cmp_ne_u32_e64 s[6:7], 1, v165
	s_andn2_b64 vcc, exec, s[0:1]
	v_mov_b32_e32 v179, v64
	v_mov_b32_e32 v180, v65
	v_mov_b32_e32 v181, v66
	v_mov_b32_e32 v182, v67
	v_mov_b32_e32 v165, v68
	v_mov_b32_e32 v167, v69
	v_mov_b32_e32 v169, v70
	v_mov_b32_e32 v171, v71
	global_store_dwordx4 v[174:175], v[184:187], off
	s_cbranch_vccnz .LBB0_253
	v_mov_b32_e32 v238, s60
	v_and_b32_e32 v214, 0x7fffffff, v64
	v_and_b32_e32 v215, 0x7fffffff, v65
	v_and_b32_e32 v220, 0x7fffffff, v66
	v_and_b32_e32 v221, 0x7fffffff, v67
	v_and_b32_e32 v226, 0x7fffffff, v68
	v_and_b32_e32 v227, 0x7fffffff, v69
	v_and_b32_e32 v232, 0x7fffffff, v70
	v_and_b32_e32 v233, 0x7fffffff, v71
	v_pk_fma_f32 v[214:215], v[214:215], s[56:57], 1.0 op_sel_hi:[1,0,0]
	v_pk_fma_f32 v[220:221], v[220:221], s[56:57], 1.0 op_sel_hi:[1,0,0]
	v_pk_fma_f32 v[226:227], v[226:227], s[56:57], 1.0 op_sel_hi:[1,0,0]
	v_pk_fma_f32 v[232:233], v[232:233], s[56:57], 1.0 op_sel_hi:[1,0,0]
	v_pk_mul_f32 v[218:219], v[64:65], v[64:65]
	v_pk_mul_f32 v[224:225], v[66:67], v[66:67]
	v_pk_mul_f32 v[230:231], v[68:69], v[68:69]
	v_pk_mul_f32 v[236:237], v[70:71], v[70:71]
	v_rcp_f32_e32 v214, v214
	v_rcp_f32_e32 v215, v215
	v_rcp_f32_e32 v220, v220
	v_rcp_f32_e32 v221, v221
	v_rcp_f32_e32 v226, v226
	v_rcp_f32_e32 v227, v227
	v_rcp_f32_e32 v232, v232
	v_rcp_f32_e32 v233, v233
	v_pk_mul_f32 v[218:219], v[218:219], s[68:69] op_sel_hi:[1,0]
	v_pk_mul_f32 v[224:225], v[224:225], s[68:69] op_sel_hi:[1,0]
	v_pk_mul_f32 v[230:231], v[230:231], s[68:69] op_sel_hi:[1,0]
	v_pk_mul_f32 v[236:237], v[236:237], s[68:69] op_sel_hi:[1,0]
	v_pk_fma_f32 v[216:217], v[214:215], s[58:59], v[238:239] op_sel_hi:[1,0,0]
	v_pk_fma_f32 v[222:223], v[220:221], s[58:59], v[238:239] op_sel_hi:[1,0,0]
	v_pk_fma_f32 v[228:229], v[226:227], s[58:59], v[238:239] op_sel_hi:[1,0,0]
	v_pk_fma_f32 v[234:235], v[232:233], s[58:59], v[238:239] op_sel_hi:[1,0,0]
	v_exp_f32_e32 v218, v218
	v_exp_f32_e32 v219, v219
	v_exp_f32_e32 v224, v224
	v_exp_f32_e32 v225, v225
	v_exp_f32_e32 v230, v230
	v_exp_f32_e32 v231, v231
	v_exp_f32_e32 v236, v236
	v_exp_f32_e32 v237, v237
	v_pk_fma_f32 v[216:217], v[214:215], v[216:217], s[62:63] op_sel_hi:[1,1,0]
	v_pk_fma_f32 v[222:223], v[220:221], v[222:223], s[62:63] op_sel_hi:[1,1,0]
	v_pk_fma_f32 v[228:229], v[226:227], v[228:229], s[62:63] op_sel_hi:[1,1,0]
	v_pk_fma_f32 v[234:235], v[232:233], v[234:235], s[62:63] op_sel_hi:[1,1,0]
	v_pk_fma_f32 v[216:217], v[214:215], v[216:217], s[64:65] op_sel_hi:[1,1,0]
	v_pk_fma_f32 v[222:223], v[220:221], v[222:223], s[64:65] op_sel_hi:[1,1,0]
	v_pk_fma_f32 v[228:229], v[226:227], v[228:229], s[64:65] op_sel_hi:[1,1,0]
	v_pk_fma_f32 v[234:235], v[232:233], v[234:235], s[64:65] op_sel_hi:[1,1,0]
	v_pk_fma_f32 v[216:217], v[214:215], v[216:217], s[66:67] op_sel_hi:[1,1,0]
	v_pk_fma_f32 v[222:223], v[220:221], v[222:223], s[66:67] op_sel_hi:[1,1,0]
	v_pk_fma_f32 v[228:229], v[226:227], v[228:229], s[66:67] op_sel_hi:[1,1,0]
	v_pk_fma_f32 v[234:235], v[232:233], v[234:235], s[66:67] op_sel_hi:[1,1,0]
	v_pk_mul_f32 v[216:217], v[214:215], v[216:217]
	v_pk_mul_f32 v[222:223], v[220:221], v[222:223]
	v_pk_mul_f32 v[228:229], v[226:227], v[228:229]
	v_pk_mul_f32 v[234:235], v[232:233], v[234:235]
	v_pk_mul_f32 v[216:217], v[218:219], v[216:217]
	v_pk_mul_f32 v[222:223], v[224:225], v[222:223]
	v_pk_mul_f32 v[228:229], v[230:231], v[228:229]
	v_pk_mul_f32 v[234:235], v[236:237], v[234:235]
	v_pk_mul_f32 v[214:215], v[64:65], v[216:217]
	v_pk_mul_f32 v[220:221], v[66:67], v[222:223]
	v_pk_mul_f32 v[226:227], v[68:69], v[228:229]
	v_pk_mul_f32 v[232:233], v[70:71], v[234:235]
	v_pk_fma_f32 v[218:219], v[64:65], v[216:217], v[64:65] neg_lo:[1,0,0] neg_hi:[1,0,0]
	v_pk_fma_f32 v[224:225], v[66:67], v[222:223], v[66:67] neg_lo:[1,0,0] neg_hi:[1,0,0]
	v_pk_fma_f32 v[230:231], v[68:69], v[228:229], v[68:69] neg_lo:[1,0,0] neg_hi:[1,0,0]
	v_pk_fma_f32 v[236:237], v[70:71], v[234:235], v[70:71] neg_lo:[1,0,0] neg_hi:[1,0,0]
	v_ashrrev_i32_e32 v216, 31, v64
	v_ashrrev_i32_e32 v217, 31, v65
	v_ashrrev_i32_e32 v222, 31, v66
	v_ashrrev_i32_e32 v223, 31, v67
	v_ashrrev_i32_e32 v228, 31, v68
	v_ashrrev_i32_e32 v229, 31, v69
	v_ashrrev_i32_e32 v234, 31, v70
	v_ashrrev_i32_e32 v235, 31, v71
	v_bfi_b32 v179, v216, v214, v218
	v_bfi_b32 v180, v217, v215, v219
	v_bfi_b32 v181, v222, v220, v224
	v_bfi_b32 v182, v223, v221, v225
	v_bfi_b32 v165, v228, v226, v230
	v_bfi_b32 v167, v229, v227, v231
	v_bfi_b32 v169, v234, v232, v236
	v_bfi_b32 v171, v235, v233, v237
.LBB0_253:
	s_nop 0
	v_cvt_pk_bf16_f32 v184, v165, v167
	v_cvt_pk_bf16_f32 v185, v169, v171
	v_cvt_pk_bf16_f32 v186, v179, v180
	v_cvt_pk_bf16_f32 v187, v181, v182
	s_and_b64 vcc, exec, s[6:7]
	v_mov_b32_e32 v179, v88
	v_mov_b32_e32 v180, v89
	v_mov_b32_e32 v181, v90
	v_mov_b32_e32 v182, v91
	v_mov_b32_e32 v165, v92
	v_mov_b32_e32 v167, v93
	v_mov_b32_e32 v169, v94
	v_mov_b32_e32 v171, v95
	global_store_dwordx4 v[174:175], v[184:187], off offset:16
	s_cbranch_vccnz .LBB0_255
	v_mov_b32_e32 v238, s60
	v_and_b32_e32 v214, 0x7fffffff, v88
	v_and_b32_e32 v215, 0x7fffffff, v89
	v_and_b32_e32 v220, 0x7fffffff, v90
	v_and_b32_e32 v221, 0x7fffffff, v91
	v_and_b32_e32 v226, 0x7fffffff, v92
	v_and_b32_e32 v227, 0x7fffffff, v93
	v_and_b32_e32 v232, 0x7fffffff, v94
	v_and_b32_e32 v233, 0x7fffffff, v95
	v_pk_fma_f32 v[214:215], v[214:215], s[56:57], 1.0 op_sel_hi:[1,0,0]
	v_pk_fma_f32 v[220:221], v[220:221], s[56:57], 1.0 op_sel_hi:[1,0,0]
	v_pk_fma_f32 v[226:227], v[226:227], s[56:57], 1.0 op_sel_hi:[1,0,0]
	v_pk_fma_f32 v[232:233], v[232:233], s[56:57], 1.0 op_sel_hi:[1,0,0]
	v_pk_mul_f32 v[218:219], v[88:89], v[88:89]
	v_pk_mul_f32 v[224:225], v[90:91], v[90:91]
	v_pk_mul_f32 v[230:231], v[92:93], v[92:93]
	v_pk_mul_f32 v[236:237], v[94:95], v[94:95]
	v_rcp_f32_e32 v214, v214
	v_rcp_f32_e32 v215, v215
	v_rcp_f32_e32 v220, v220
	v_rcp_f32_e32 v221, v221
	v_rcp_f32_e32 v226, v226
	v_rcp_f32_e32 v227, v227
	v_rcp_f32_e32 v232, v232
	v_rcp_f32_e32 v233, v233
	v_pk_mul_f32 v[218:219], v[218:219], s[68:69] op_sel_hi:[1,0]
	v_pk_mul_f32 v[224:225], v[224:225], s[68:69] op_sel_hi:[1,0]
	v_pk_mul_f32 v[230:231], v[230:231], s[68:69] op_sel_hi:[1,0]
	v_pk_mul_f32 v[236:237], v[236:237], s[68:69] op_sel_hi:[1,0]
	v_pk_fma_f32 v[216:217], v[214:215], s[58:59], v[238:239] op_sel_hi:[1,0,0]
	v_pk_fma_f32 v[222:223], v[220:221], s[58:59], v[238:239] op_sel_hi:[1,0,0]
	v_pk_fma_f32 v[228:229], v[226:227], s[58:59], v[238:239] op_sel_hi:[1,0,0]
	v_pk_fma_f32 v[234:235], v[232:233], s[58:59], v[238:239] op_sel_hi:[1,0,0]
	v_exp_f32_e32 v218, v218
	v_exp_f32_e32 v219, v219
	v_exp_f32_e32 v224, v224
	v_exp_f32_e32 v225, v225
	v_exp_f32_e32 v230, v230
	v_exp_f32_e32 v231, v231
	v_exp_f32_e32 v236, v236
	v_exp_f32_e32 v237, v237
	v_pk_fma_f32 v[216:217], v[214:215], v[216:217], s[62:63] op_sel_hi:[1,1,0]
	v_pk_fma_f32 v[222:223], v[220:221], v[222:223], s[62:63] op_sel_hi:[1,1,0]
	v_pk_fma_f32 v[228:229], v[226:227], v[228:229], s[62:63] op_sel_hi:[1,1,0]
	v_pk_fma_f32 v[234:235], v[232:233], v[234:235], s[62:63] op_sel_hi:[1,1,0]
	v_pk_fma_f32 v[216:217], v[214:215], v[216:217], s[64:65] op_sel_hi:[1,1,0]
	v_pk_fma_f32 v[222:223], v[220:221], v[222:223], s[64:65] op_sel_hi:[1,1,0]
	v_pk_fma_f32 v[228:229], v[226:227], v[228:229], s[64:65] op_sel_hi:[1,1,0]
	v_pk_fma_f32 v[234:235], v[232:233], v[234:235], s[64:65] op_sel_hi:[1,1,0]
	v_pk_fma_f32 v[216:217], v[214:215], v[216:217], s[66:67] op_sel_hi:[1,1,0]
	v_pk_fma_f32 v[222:223], v[220:221], v[222:223], s[66:67] op_sel_hi:[1,1,0]
	v_pk_fma_f32 v[228:229], v[226:227], v[228:229], s[66:67] op_sel_hi:[1,1,0]
	v_pk_fma_f32 v[234:235], v[232:233], v[234:235], s[66:67] op_sel_hi:[1,1,0]
	v_pk_mul_f32 v[216:217], v[214:215], v[216:217]
	v_pk_mul_f32 v[222:223], v[220:221], v[222:223]
	v_pk_mul_f32 v[228:229], v[226:227], v[228:229]
	v_pk_mul_f32 v[234:235], v[232:233], v[234:235]
	v_pk_mul_f32 v[216:217], v[218:219], v[216:217]
	v_pk_mul_f32 v[222:223], v[224:225], v[222:223]
	v_pk_mul_f32 v[228:229], v[230:231], v[228:229]
	v_pk_mul_f32 v[234:235], v[236:237], v[234:235]
	v_pk_mul_f32 v[214:215], v[88:89], v[216:217]
	v_pk_mul_f32 v[220:221], v[90:91], v[222:223]
	v_pk_mul_f32 v[226:227], v[92:93], v[228:229]
	v_pk_mul_f32 v[232:233], v[94:95], v[234:235]
	v_pk_fma_f32 v[218:219], v[88:89], v[216:217], v[88:89] neg_lo:[1,0,0] neg_hi:[1,0,0]
	v_pk_fma_f32 v[224:225], v[90:91], v[222:223], v[90:91] neg_lo:[1,0,0] neg_hi:[1,0,0]
	v_pk_fma_f32 v[230:231], v[92:93], v[228:229], v[92:93] neg_lo:[1,0,0] neg_hi:[1,0,0]
	v_pk_fma_f32 v[236:237], v[94:95], v[234:235], v[94:95] neg_lo:[1,0,0] neg_hi:[1,0,0]
	v_ashrrev_i32_e32 v216, 31, v88
	v_ashrrev_i32_e32 v217, 31, v89
	v_ashrrev_i32_e32 v222, 31, v90
	v_ashrrev_i32_e32 v223, 31, v91
	v_ashrrev_i32_e32 v228, 31, v92
	v_ashrrev_i32_e32 v229, 31, v93
	v_ashrrev_i32_e32 v234, 31, v94
	v_ashrrev_i32_e32 v235, 31, v95
	v_bfi_b32 v179, v216, v214, v218
	v_bfi_b32 v180, v217, v215, v219
	v_bfi_b32 v181, v222, v220, v224
	v_bfi_b32 v182, v223, v221, v225
	v_bfi_b32 v165, v228, v226, v230
	v_bfi_b32 v167, v229, v227, v231
	v_bfi_b32 v169, v234, v232, v236
	v_bfi_b32 v171, v235, v233, v237
.LBB0_255:
	v_or_b32_e32 v174, 16, v163
	v_mad_i64_i32 v[174:175], s[0:1], v174, s94, v[172:173]
	v_cvt_pk_bf16_f32 v184, v165, v167
	v_cvt_pk_bf16_f32 v185, v169, v171
	v_cvt_pk_bf16_f32 v186, v179, v180
	v_cvt_pk_bf16_f32 v187, v181, v182
	s_and_b64 vcc, exec, s[6:7]
	v_mov_b32_e32 v179, v56
	v_mov_b32_e32 v180, v57
	v_mov_b32_e32 v181, v58
	v_mov_b32_e32 v182, v59
	v_mov_b32_e32 v165, v60
	v_mov_b32_e32 v167, v61
	v_mov_b32_e32 v169, v62
	v_mov_b32_e32 v171, v63
	global_store_dwordx4 v[174:175], v[184:187], off
	s_cbranch_vccnz .LBB0_257
	v_mov_b32_e32 v238, s60
	v_and_b32_e32 v214, 0x7fffffff, v56
	v_and_b32_e32 v215, 0x7fffffff, v57
	v_and_b32_e32 v220, 0x7fffffff, v58
	v_and_b32_e32 v221, 0x7fffffff, v59
	v_and_b32_e32 v226, 0x7fffffff, v60
	v_and_b32_e32 v227, 0x7fffffff, v61
	v_and_b32_e32 v232, 0x7fffffff, v62
	v_and_b32_e32 v233, 0x7fffffff, v63
	v_pk_fma_f32 v[214:215], v[214:215], s[56:57], 1.0 op_sel_hi:[1,0,0]
	v_pk_fma_f32 v[220:221], v[220:221], s[56:57], 1.0 op_sel_hi:[1,0,0]
	v_pk_fma_f32 v[226:227], v[226:227], s[56:57], 1.0 op_sel_hi:[1,0,0]
	v_pk_fma_f32 v[232:233], v[232:233], s[56:57], 1.0 op_sel_hi:[1,0,0]
	v_pk_mul_f32 v[218:219], v[56:57], v[56:57]
	v_pk_mul_f32 v[224:225], v[58:59], v[58:59]
	v_pk_mul_f32 v[230:231], v[60:61], v[60:61]
	v_pk_mul_f32 v[236:237], v[62:63], v[62:63]
	v_rcp_f32_e32 v214, v214
	v_rcp_f32_e32 v215, v215
	v_rcp_f32_e32 v220, v220
	v_rcp_f32_e32 v221, v221
	v_rcp_f32_e32 v226, v226
	v_rcp_f32_e32 v227, v227
	v_rcp_f32_e32 v232, v232
	v_rcp_f32_e32 v233, v233
	v_pk_mul_f32 v[218:219], v[218:219], s[68:69] op_sel_hi:[1,0]
	v_pk_mul_f32 v[224:225], v[224:225], s[68:69] op_sel_hi:[1,0]
	v_pk_mul_f32 v[230:231], v[230:231], s[68:69] op_sel_hi:[1,0]
	v_pk_mul_f32 v[236:237], v[236:237], s[68:69] op_sel_hi:[1,0]
	v_pk_fma_f32 v[216:217], v[214:215], s[58:59], v[238:239] op_sel_hi:[1,0,0]
	v_pk_fma_f32 v[222:223], v[220:221], s[58:59], v[238:239] op_sel_hi:[1,0,0]
	v_pk_fma_f32 v[228:229], v[226:227], s[58:59], v[238:239] op_sel_hi:[1,0,0]
	v_pk_fma_f32 v[234:235], v[232:233], s[58:59], v[238:239] op_sel_hi:[1,0,0]
	v_exp_f32_e32 v218, v218
	v_exp_f32_e32 v219, v219
	v_exp_f32_e32 v224, v224
	v_exp_f32_e32 v225, v225
	v_exp_f32_e32 v230, v230
	v_exp_f32_e32 v231, v231
	v_exp_f32_e32 v236, v236
	v_exp_f32_e32 v237, v237
	v_pk_fma_f32 v[216:217], v[214:215], v[216:217], s[62:63] op_sel_hi:[1,1,0]
	v_pk_fma_f32 v[222:223], v[220:221], v[222:223], s[62:63] op_sel_hi:[1,1,0]
	v_pk_fma_f32 v[228:229], v[226:227], v[228:229], s[62:63] op_sel_hi:[1,1,0]
	v_pk_fma_f32 v[234:235], v[232:233], v[234:235], s[62:63] op_sel_hi:[1,1,0]
	v_pk_fma_f32 v[216:217], v[214:215], v[216:217], s[64:65] op_sel_hi:[1,1,0]
	v_pk_fma_f32 v[222:223], v[220:221], v[222:223], s[64:65] op_sel_hi:[1,1,0]
	v_pk_fma_f32 v[228:229], v[226:227], v[228:229], s[64:65] op_sel_hi:[1,1,0]
	v_pk_fma_f32 v[234:235], v[232:233], v[234:235], s[64:65] op_sel_hi:[1,1,0]
	v_pk_fma_f32 v[216:217], v[214:215], v[216:217], s[66:67] op_sel_hi:[1,1,0]
	v_pk_fma_f32 v[222:223], v[220:221], v[222:223], s[66:67] op_sel_hi:[1,1,0]
	v_pk_fma_f32 v[228:229], v[226:227], v[228:229], s[66:67] op_sel_hi:[1,1,0]
	v_pk_fma_f32 v[234:235], v[232:233], v[234:235], s[66:67] op_sel_hi:[1,1,0]
	v_pk_mul_f32 v[216:217], v[214:215], v[216:217]
	v_pk_mul_f32 v[222:223], v[220:221], v[222:223]
	v_pk_mul_f32 v[228:229], v[226:227], v[228:229]
	v_pk_mul_f32 v[234:235], v[232:233], v[234:235]
	v_pk_mul_f32 v[216:217], v[218:219], v[216:217]
	v_pk_mul_f32 v[222:223], v[224:225], v[222:223]
	v_pk_mul_f32 v[228:229], v[230:231], v[228:229]
	v_pk_mul_f32 v[234:235], v[236:237], v[234:235]
	v_pk_mul_f32 v[214:215], v[56:57], v[216:217]
	v_pk_mul_f32 v[220:221], v[58:59], v[222:223]
	v_pk_mul_f32 v[226:227], v[60:61], v[228:229]
	v_pk_mul_f32 v[232:233], v[62:63], v[234:235]
	v_pk_fma_f32 v[218:219], v[56:57], v[216:217], v[56:57] neg_lo:[1,0,0] neg_hi:[1,0,0]
	v_pk_fma_f32 v[224:225], v[58:59], v[222:223], v[58:59] neg_lo:[1,0,0] neg_hi:[1,0,0]
	v_pk_fma_f32 v[230:231], v[60:61], v[228:229], v[60:61] neg_lo:[1,0,0] neg_hi:[1,0,0]
	v_pk_fma_f32 v[236:237], v[62:63], v[234:235], v[62:63] neg_lo:[1,0,0] neg_hi:[1,0,0]
	v_ashrrev_i32_e32 v216, 31, v56
	v_ashrrev_i32_e32 v217, 31, v57
	v_ashrrev_i32_e32 v222, 31, v58
	v_ashrrev_i32_e32 v223, 31, v59
	v_ashrrev_i32_e32 v228, 31, v60
	v_ashrrev_i32_e32 v229, 31, v61
	v_ashrrev_i32_e32 v234, 31, v62
	v_ashrrev_i32_e32 v235, 31, v63
	v_bfi_b32 v179, v216, v214, v218
	v_bfi_b32 v180, v217, v215, v219
	v_bfi_b32 v181, v222, v220, v224
	v_bfi_b32 v182, v223, v221, v225
	v_bfi_b32 v165, v228, v226, v230
	v_bfi_b32 v167, v229, v227, v231
	v_bfi_b32 v169, v234, v232, v236
	v_bfi_b32 v171, v235, v233, v237
.LBB0_257:
	s_nop 0
	v_cvt_pk_bf16_f32 v184, v165, v167
	v_cvt_pk_bf16_f32 v185, v169, v171
	v_cvt_pk_bf16_f32 v186, v179, v180
	v_cvt_pk_bf16_f32 v187, v181, v182
	s_and_b64 vcc, exec, s[6:7]
	v_mov_b32_e32 v179, v80
	v_mov_b32_e32 v180, v81
	v_mov_b32_e32 v181, v82
	v_mov_b32_e32 v182, v83
	v_mov_b32_e32 v165, v84
	v_mov_b32_e32 v167, v85
	v_mov_b32_e32 v169, v86
	v_mov_b32_e32 v171, v87
	global_store_dwordx4 v[174:175], v[184:187], off offset:16
	s_cbranch_vccnz .LBB0_259
	v_mov_b32_e32 v238, s60
	v_and_b32_e32 v214, 0x7fffffff, v80
	v_and_b32_e32 v215, 0x7fffffff, v81
	v_and_b32_e32 v220, 0x7fffffff, v82
	v_and_b32_e32 v221, 0x7fffffff, v83
	v_and_b32_e32 v226, 0x7fffffff, v84
	v_and_b32_e32 v227, 0x7fffffff, v85
	v_and_b32_e32 v232, 0x7fffffff, v86
	v_and_b32_e32 v233, 0x7fffffff, v87
	v_pk_fma_f32 v[214:215], v[214:215], s[56:57], 1.0 op_sel_hi:[1,0,0]
	v_pk_fma_f32 v[220:221], v[220:221], s[56:57], 1.0 op_sel_hi:[1,0,0]
	v_pk_fma_f32 v[226:227], v[226:227], s[56:57], 1.0 op_sel_hi:[1,0,0]
	v_pk_fma_f32 v[232:233], v[232:233], s[56:57], 1.0 op_sel_hi:[1,0,0]
	v_pk_mul_f32 v[218:219], v[80:81], v[80:81]
	v_pk_mul_f32 v[224:225], v[82:83], v[82:83]
	v_pk_mul_f32 v[230:231], v[84:85], v[84:85]
	v_pk_mul_f32 v[236:237], v[86:87], v[86:87]
	v_rcp_f32_e32 v214, v214
	v_rcp_f32_e32 v215, v215
	v_rcp_f32_e32 v220, v220
	v_rcp_f32_e32 v221, v221
	v_rcp_f32_e32 v226, v226
	v_rcp_f32_e32 v227, v227
	v_rcp_f32_e32 v232, v232
	v_rcp_f32_e32 v233, v233
	v_pk_mul_f32 v[218:219], v[218:219], s[68:69] op_sel_hi:[1,0]
	v_pk_mul_f32 v[224:225], v[224:225], s[68:69] op_sel_hi:[1,0]
	v_pk_mul_f32 v[230:231], v[230:231], s[68:69] op_sel_hi:[1,0]
	v_pk_mul_f32 v[236:237], v[236:237], s[68:69] op_sel_hi:[1,0]
	v_pk_fma_f32 v[216:217], v[214:215], s[58:59], v[238:239] op_sel_hi:[1,0,0]
	v_pk_fma_f32 v[222:223], v[220:221], s[58:59], v[238:239] op_sel_hi:[1,0,0]
	v_pk_fma_f32 v[228:229], v[226:227], s[58:59], v[238:239] op_sel_hi:[1,0,0]
	v_pk_fma_f32 v[234:235], v[232:233], s[58:59], v[238:239] op_sel_hi:[1,0,0]
	v_exp_f32_e32 v218, v218
	v_exp_f32_e32 v219, v219
	v_exp_f32_e32 v224, v224
	v_exp_f32_e32 v225, v225
	v_exp_f32_e32 v230, v230
	v_exp_f32_e32 v231, v231
	v_exp_f32_e32 v236, v236
	v_exp_f32_e32 v237, v237
	v_pk_fma_f32 v[216:217], v[214:215], v[216:217], s[62:63] op_sel_hi:[1,1,0]
	v_pk_fma_f32 v[222:223], v[220:221], v[222:223], s[62:63] op_sel_hi:[1,1,0]
	v_pk_fma_f32 v[228:229], v[226:227], v[228:229], s[62:63] op_sel_hi:[1,1,0]
	v_pk_fma_f32 v[234:235], v[232:233], v[234:235], s[62:63] op_sel_hi:[1,1,0]
	v_pk_fma_f32 v[216:217], v[214:215], v[216:217], s[64:65] op_sel_hi:[1,1,0]
	v_pk_fma_f32 v[222:223], v[220:221], v[222:223], s[64:65] op_sel_hi:[1,1,0]
	v_pk_fma_f32 v[228:229], v[226:227], v[228:229], s[64:65] op_sel_hi:[1,1,0]
	v_pk_fma_f32 v[234:235], v[232:233], v[234:235], s[64:65] op_sel_hi:[1,1,0]
	v_pk_fma_f32 v[216:217], v[214:215], v[216:217], s[66:67] op_sel_hi:[1,1,0]
	v_pk_fma_f32 v[222:223], v[220:221], v[222:223], s[66:67] op_sel_hi:[1,1,0]
	v_pk_fma_f32 v[228:229], v[226:227], v[228:229], s[66:67] op_sel_hi:[1,1,0]
	v_pk_fma_f32 v[234:235], v[232:233], v[234:235], s[66:67] op_sel_hi:[1,1,0]
	v_pk_mul_f32 v[216:217], v[214:215], v[216:217]
	v_pk_mul_f32 v[222:223], v[220:221], v[222:223]
	v_pk_mul_f32 v[228:229], v[226:227], v[228:229]
	v_pk_mul_f32 v[234:235], v[232:233], v[234:235]
	v_pk_mul_f32 v[216:217], v[218:219], v[216:217]
	v_pk_mul_f32 v[222:223], v[224:225], v[222:223]
	v_pk_mul_f32 v[228:229], v[230:231], v[228:229]
	v_pk_mul_f32 v[234:235], v[236:237], v[234:235]
	v_pk_mul_f32 v[214:215], v[80:81], v[216:217]
	v_pk_mul_f32 v[220:221], v[82:83], v[222:223]
	v_pk_mul_f32 v[226:227], v[84:85], v[228:229]
	v_pk_mul_f32 v[232:233], v[86:87], v[234:235]
	v_pk_fma_f32 v[218:219], v[80:81], v[216:217], v[80:81] neg_lo:[1,0,0] neg_hi:[1,0,0]
	v_pk_fma_f32 v[224:225], v[82:83], v[222:223], v[82:83] neg_lo:[1,0,0] neg_hi:[1,0,0]
	v_pk_fma_f32 v[230:231], v[84:85], v[228:229], v[84:85] neg_lo:[1,0,0] neg_hi:[1,0,0]
	v_pk_fma_f32 v[236:237], v[86:87], v[234:235], v[86:87] neg_lo:[1,0,0] neg_hi:[1,0,0]
	v_ashrrev_i32_e32 v216, 31, v80
	v_ashrrev_i32_e32 v217, 31, v81
	v_ashrrev_i32_e32 v222, 31, v82
	v_ashrrev_i32_e32 v223, 31, v83
	v_ashrrev_i32_e32 v228, 31, v84
	v_ashrrev_i32_e32 v229, 31, v85
	v_ashrrev_i32_e32 v234, 31, v86
	v_ashrrev_i32_e32 v235, 31, v87
	v_bfi_b32 v179, v216, v214, v218
	v_bfi_b32 v180, v217, v215, v219
	v_bfi_b32 v181, v222, v220, v224
	v_bfi_b32 v182, v223, v221, v225
	v_bfi_b32 v165, v228, v226, v230
	v_bfi_b32 v167, v229, v227, v231
	v_bfi_b32 v169, v234, v232, v236
	v_bfi_b32 v171, v235, v233, v237
.LBB0_259:
	v_or_b32_e32 v174, 32, v163
	v_mad_i64_i32 v[174:175], s[0:1], v174, s94, v[172:173]
	v_cvt_pk_bf16_f32 v184, v165, v167
	v_cvt_pk_bf16_f32 v185, v169, v171
	v_cvt_pk_bf16_f32 v186, v179, v180
	v_cvt_pk_bf16_f32 v187, v181, v182
	s_and_b64 vcc, exec, s[6:7]
	v_mov_b32_e32 v179, v48
	v_mov_b32_e32 v180, v49
	v_mov_b32_e32 v181, v50
	v_mov_b32_e32 v182, v51
	v_mov_b32_e32 v165, v52
	v_mov_b32_e32 v167, v53
	v_mov_b32_e32 v169, v54
	v_mov_b32_e32 v171, v55
	global_store_dwordx4 v[174:175], v[184:187], off
	s_cbranch_vccnz .LBB0_261
	v_mov_b32_e32 v238, s60
	v_and_b32_e32 v214, 0x7fffffff, v48
	v_and_b32_e32 v215, 0x7fffffff, v49
	v_and_b32_e32 v220, 0x7fffffff, v50
	v_and_b32_e32 v221, 0x7fffffff, v51
	v_and_b32_e32 v226, 0x7fffffff, v52
	v_and_b32_e32 v227, 0x7fffffff, v53
	v_and_b32_e32 v232, 0x7fffffff, v54
	v_and_b32_e32 v233, 0x7fffffff, v55
	v_pk_fma_f32 v[214:215], v[214:215], s[56:57], 1.0 op_sel_hi:[1,0,0]
	v_pk_fma_f32 v[220:221], v[220:221], s[56:57], 1.0 op_sel_hi:[1,0,0]
	v_pk_fma_f32 v[226:227], v[226:227], s[56:57], 1.0 op_sel_hi:[1,0,0]
	v_pk_fma_f32 v[232:233], v[232:233], s[56:57], 1.0 op_sel_hi:[1,0,0]
	v_pk_mul_f32 v[218:219], v[48:49], v[48:49]
	v_pk_mul_f32 v[224:225], v[50:51], v[50:51]
	v_pk_mul_f32 v[230:231], v[52:53], v[52:53]
	v_pk_mul_f32 v[236:237], v[54:55], v[54:55]
	v_rcp_f32_e32 v214, v214
	v_rcp_f32_e32 v215, v215
	v_rcp_f32_e32 v220, v220
	v_rcp_f32_e32 v221, v221
	v_rcp_f32_e32 v226, v226
	v_rcp_f32_e32 v227, v227
	v_rcp_f32_e32 v232, v232
	v_rcp_f32_e32 v233, v233
	v_pk_mul_f32 v[218:219], v[218:219], s[68:69] op_sel_hi:[1,0]
	v_pk_mul_f32 v[224:225], v[224:225], s[68:69] op_sel_hi:[1,0]
	v_pk_mul_f32 v[230:231], v[230:231], s[68:69] op_sel_hi:[1,0]
	v_pk_mul_f32 v[236:237], v[236:237], s[68:69] op_sel_hi:[1,0]
	v_pk_fma_f32 v[216:217], v[214:215], s[58:59], v[238:239] op_sel_hi:[1,0,0]
	v_pk_fma_f32 v[222:223], v[220:221], s[58:59], v[238:239] op_sel_hi:[1,0,0]
	v_pk_fma_f32 v[228:229], v[226:227], s[58:59], v[238:239] op_sel_hi:[1,0,0]
	v_pk_fma_f32 v[234:235], v[232:233], s[58:59], v[238:239] op_sel_hi:[1,0,0]
	v_exp_f32_e32 v218, v218
	v_exp_f32_e32 v219, v219
	v_exp_f32_e32 v224, v224
	v_exp_f32_e32 v225, v225
	v_exp_f32_e32 v230, v230
	v_exp_f32_e32 v231, v231
	v_exp_f32_e32 v236, v236
	v_exp_f32_e32 v237, v237
	v_pk_fma_f32 v[216:217], v[214:215], v[216:217], s[62:63] op_sel_hi:[1,1,0]
	v_pk_fma_f32 v[222:223], v[220:221], v[222:223], s[62:63] op_sel_hi:[1,1,0]
	v_pk_fma_f32 v[228:229], v[226:227], v[228:229], s[62:63] op_sel_hi:[1,1,0]
	v_pk_fma_f32 v[234:235], v[232:233], v[234:235], s[62:63] op_sel_hi:[1,1,0]
	v_pk_fma_f32 v[216:217], v[214:215], v[216:217], s[64:65] op_sel_hi:[1,1,0]
	v_pk_fma_f32 v[222:223], v[220:221], v[222:223], s[64:65] op_sel_hi:[1,1,0]
	v_pk_fma_f32 v[228:229], v[226:227], v[228:229], s[64:65] op_sel_hi:[1,1,0]
	v_pk_fma_f32 v[234:235], v[232:233], v[234:235], s[64:65] op_sel_hi:[1,1,0]
	v_pk_fma_f32 v[216:217], v[214:215], v[216:217], s[66:67] op_sel_hi:[1,1,0]
	v_pk_fma_f32 v[222:223], v[220:221], v[222:223], s[66:67] op_sel_hi:[1,1,0]
	v_pk_fma_f32 v[228:229], v[226:227], v[228:229], s[66:67] op_sel_hi:[1,1,0]
	v_pk_fma_f32 v[234:235], v[232:233], v[234:235], s[66:67] op_sel_hi:[1,1,0]
	v_pk_mul_f32 v[216:217], v[214:215], v[216:217]
	v_pk_mul_f32 v[222:223], v[220:221], v[222:223]
	v_pk_mul_f32 v[228:229], v[226:227], v[228:229]
	v_pk_mul_f32 v[234:235], v[232:233], v[234:235]
	v_pk_mul_f32 v[216:217], v[218:219], v[216:217]
	v_pk_mul_f32 v[222:223], v[224:225], v[222:223]
	v_pk_mul_f32 v[228:229], v[230:231], v[228:229]
	v_pk_mul_f32 v[234:235], v[236:237], v[234:235]
	v_pk_mul_f32 v[214:215], v[48:49], v[216:217]
	v_pk_mul_f32 v[220:221], v[50:51], v[222:223]
	v_pk_mul_f32 v[226:227], v[52:53], v[228:229]
	v_pk_mul_f32 v[232:233], v[54:55], v[234:235]
	v_pk_fma_f32 v[218:219], v[48:49], v[216:217], v[48:49] neg_lo:[1,0,0] neg_hi:[1,0,0]
	v_pk_fma_f32 v[224:225], v[50:51], v[222:223], v[50:51] neg_lo:[1,0,0] neg_hi:[1,0,0]
	v_pk_fma_f32 v[230:231], v[52:53], v[228:229], v[52:53] neg_lo:[1,0,0] neg_hi:[1,0,0]
	v_pk_fma_f32 v[236:237], v[54:55], v[234:235], v[54:55] neg_lo:[1,0,0] neg_hi:[1,0,0]
	v_ashrrev_i32_e32 v216, 31, v48
	v_ashrrev_i32_e32 v217, 31, v49
	v_ashrrev_i32_e32 v222, 31, v50
	v_ashrrev_i32_e32 v223, 31, v51
	v_ashrrev_i32_e32 v228, 31, v52
	v_ashrrev_i32_e32 v229, 31, v53
	v_ashrrev_i32_e32 v234, 31, v54
	v_ashrrev_i32_e32 v235, 31, v55
	v_bfi_b32 v179, v216, v214, v218
	v_bfi_b32 v180, v217, v215, v219
	v_bfi_b32 v181, v222, v220, v224
	v_bfi_b32 v182, v223, v221, v225
	v_bfi_b32 v165, v228, v226, v230
	v_bfi_b32 v167, v229, v227, v231
	v_bfi_b32 v169, v234, v232, v236
	v_bfi_b32 v171, v235, v233, v237
.LBB0_261:
	s_nop 0
	v_cvt_pk_bf16_f32 v184, v165, v167
	v_cvt_pk_bf16_f32 v185, v169, v171
	v_cvt_pk_bf16_f32 v186, v179, v180
	v_cvt_pk_bf16_f32 v187, v181, v182
	s_and_b64 vcc, exec, s[6:7]
	v_mov_b32_e32 v179, v72
	v_mov_b32_e32 v180, v73
	v_mov_b32_e32 v181, v74
	v_mov_b32_e32 v182, v75
	v_mov_b32_e32 v165, v76
	v_mov_b32_e32 v167, v77
	v_mov_b32_e32 v169, v78
	v_mov_b32_e32 v171, v79
	global_store_dwordx4 v[174:175], v[184:187], off offset:16
	s_cbranch_vccnz .LBB0_263
	v_mov_b32_e32 v238, s60
	v_and_b32_e32 v214, 0x7fffffff, v72
	v_and_b32_e32 v215, 0x7fffffff, v73
	v_and_b32_e32 v220, 0x7fffffff, v74
	v_and_b32_e32 v221, 0x7fffffff, v75
	v_and_b32_e32 v226, 0x7fffffff, v76
	v_and_b32_e32 v227, 0x7fffffff, v77
	v_and_b32_e32 v232, 0x7fffffff, v78
	v_and_b32_e32 v233, 0x7fffffff, v79
	v_pk_fma_f32 v[214:215], v[214:215], s[56:57], 1.0 op_sel_hi:[1,0,0]
	v_pk_fma_f32 v[220:221], v[220:221], s[56:57], 1.0 op_sel_hi:[1,0,0]
	v_pk_fma_f32 v[226:227], v[226:227], s[56:57], 1.0 op_sel_hi:[1,0,0]
	v_pk_fma_f32 v[232:233], v[232:233], s[56:57], 1.0 op_sel_hi:[1,0,0]
	v_pk_mul_f32 v[218:219], v[72:73], v[72:73]
	v_pk_mul_f32 v[224:225], v[74:75], v[74:75]
	v_pk_mul_f32 v[230:231], v[76:77], v[76:77]
	v_pk_mul_f32 v[236:237], v[78:79], v[78:79]
	v_rcp_f32_e32 v214, v214
	v_rcp_f32_e32 v215, v215
	v_rcp_f32_e32 v220, v220
	v_rcp_f32_e32 v221, v221
	v_rcp_f32_e32 v226, v226
	v_rcp_f32_e32 v227, v227
	v_rcp_f32_e32 v232, v232
	v_rcp_f32_e32 v233, v233
	v_pk_mul_f32 v[218:219], v[218:219], s[68:69] op_sel_hi:[1,0]
	v_pk_mul_f32 v[224:225], v[224:225], s[68:69] op_sel_hi:[1,0]
	v_pk_mul_f32 v[230:231], v[230:231], s[68:69] op_sel_hi:[1,0]
	v_pk_mul_f32 v[236:237], v[236:237], s[68:69] op_sel_hi:[1,0]
	v_pk_fma_f32 v[216:217], v[214:215], s[58:59], v[238:239] op_sel_hi:[1,0,0]
	v_pk_fma_f32 v[222:223], v[220:221], s[58:59], v[238:239] op_sel_hi:[1,0,0]
	v_pk_fma_f32 v[228:229], v[226:227], s[58:59], v[238:239] op_sel_hi:[1,0,0]
	v_pk_fma_f32 v[234:235], v[232:233], s[58:59], v[238:239] op_sel_hi:[1,0,0]
	v_exp_f32_e32 v218, v218
	v_exp_f32_e32 v219, v219
	v_exp_f32_e32 v224, v224
	v_exp_f32_e32 v225, v225
	v_exp_f32_e32 v230, v230
	v_exp_f32_e32 v231, v231
	v_exp_f32_e32 v236, v236
	v_exp_f32_e32 v237, v237
	v_pk_fma_f32 v[216:217], v[214:215], v[216:217], s[62:63] op_sel_hi:[1,1,0]
	v_pk_fma_f32 v[222:223], v[220:221], v[222:223], s[62:63] op_sel_hi:[1,1,0]
	v_pk_fma_f32 v[228:229], v[226:227], v[228:229], s[62:63] op_sel_hi:[1,1,0]
	v_pk_fma_f32 v[234:235], v[232:233], v[234:235], s[62:63] op_sel_hi:[1,1,0]
	v_pk_fma_f32 v[216:217], v[214:215], v[216:217], s[64:65] op_sel_hi:[1,1,0]
	v_pk_fma_f32 v[222:223], v[220:221], v[222:223], s[64:65] op_sel_hi:[1,1,0]
	v_pk_fma_f32 v[228:229], v[226:227], v[228:229], s[64:65] op_sel_hi:[1,1,0]
	v_pk_fma_f32 v[234:235], v[232:233], v[234:235], s[64:65] op_sel_hi:[1,1,0]
	v_pk_fma_f32 v[216:217], v[214:215], v[216:217], s[66:67] op_sel_hi:[1,1,0]
	v_pk_fma_f32 v[222:223], v[220:221], v[222:223], s[66:67] op_sel_hi:[1,1,0]
	v_pk_fma_f32 v[228:229], v[226:227], v[228:229], s[66:67] op_sel_hi:[1,1,0]
	v_pk_fma_f32 v[234:235], v[232:233], v[234:235], s[66:67] op_sel_hi:[1,1,0]
	v_pk_mul_f32 v[216:217], v[214:215], v[216:217]
	v_pk_mul_f32 v[222:223], v[220:221], v[222:223]
	v_pk_mul_f32 v[228:229], v[226:227], v[228:229]
	v_pk_mul_f32 v[234:235], v[232:233], v[234:235]
	v_pk_mul_f32 v[216:217], v[218:219], v[216:217]
	v_pk_mul_f32 v[222:223], v[224:225], v[222:223]
	v_pk_mul_f32 v[228:229], v[230:231], v[228:229]
	v_pk_mul_f32 v[234:235], v[236:237], v[234:235]
	v_pk_mul_f32 v[214:215], v[72:73], v[216:217]
	v_pk_mul_f32 v[220:221], v[74:75], v[222:223]
	v_pk_mul_f32 v[226:227], v[76:77], v[228:229]
	v_pk_mul_f32 v[232:233], v[78:79], v[234:235]
	v_pk_fma_f32 v[218:219], v[72:73], v[216:217], v[72:73] neg_lo:[1,0,0] neg_hi:[1,0,0]
	v_pk_fma_f32 v[224:225], v[74:75], v[222:223], v[74:75] neg_lo:[1,0,0] neg_hi:[1,0,0]
	v_pk_fma_f32 v[230:231], v[76:77], v[228:229], v[76:77] neg_lo:[1,0,0] neg_hi:[1,0,0]
	v_pk_fma_f32 v[236:237], v[78:79], v[234:235], v[78:79] neg_lo:[1,0,0] neg_hi:[1,0,0]
	v_ashrrev_i32_e32 v216, 31, v72
	v_ashrrev_i32_e32 v217, 31, v73
	v_ashrrev_i32_e32 v222, 31, v74
	v_ashrrev_i32_e32 v223, 31, v75
	v_ashrrev_i32_e32 v228, 31, v76
	v_ashrrev_i32_e32 v229, 31, v77
	v_ashrrev_i32_e32 v234, 31, v78
	v_ashrrev_i32_e32 v235, 31, v79
	v_bfi_b32 v179, v216, v214, v218
	v_bfi_b32 v180, v217, v215, v219
	v_bfi_b32 v181, v222, v220, v224
	v_bfi_b32 v182, v223, v221, v225
	v_bfi_b32 v165, v228, v226, v230
	v_bfi_b32 v167, v229, v227, v231
	v_bfi_b32 v169, v234, v232, v236
	v_bfi_b32 v171, v235, v233, v237
.LBB0_263:
	v_or_b32_e32 v174, 48, v163
	v_mad_i64_i32 v[174:175], s[0:1], v174, s94, v[172:173]
	v_cvt_pk_bf16_f32 v184, v165, v167
	v_cvt_pk_bf16_f32 v185, v169, v171
	v_cvt_pk_bf16_f32 v186, v179, v180
	v_cvt_pk_bf16_f32 v187, v181, v182
	s_and_b64 vcc, exec, s[6:7]
	v_mov_b32_e32 v179, v32
	v_mov_b32_e32 v180, v33
	v_mov_b32_e32 v181, v34
	v_mov_b32_e32 v182, v35
	v_mov_b32_e32 v165, v40
	v_mov_b32_e32 v167, v41
	v_mov_b32_e32 v169, v42
	v_mov_b32_e32 v171, v43
	global_store_dwordx4 v[174:175], v[184:187], off
	s_cbranch_vccnz .LBB0_265
	v_mov_b32_e32 v238, s60
	v_and_b32_e32 v214, 0x7fffffff, v32
	v_and_b32_e32 v215, 0x7fffffff, v33
	v_and_b32_e32 v220, 0x7fffffff, v34
	v_and_b32_e32 v221, 0x7fffffff, v35
	v_and_b32_e32 v226, 0x7fffffff, v40
	v_and_b32_e32 v227, 0x7fffffff, v41
	v_and_b32_e32 v232, 0x7fffffff, v42
	v_and_b32_e32 v233, 0x7fffffff, v43
	v_pk_fma_f32 v[214:215], v[214:215], s[56:57], 1.0 op_sel_hi:[1,0,0]
	v_pk_fma_f32 v[220:221], v[220:221], s[56:57], 1.0 op_sel_hi:[1,0,0]
	v_pk_fma_f32 v[226:227], v[226:227], s[56:57], 1.0 op_sel_hi:[1,0,0]
	v_pk_fma_f32 v[232:233], v[232:233], s[56:57], 1.0 op_sel_hi:[1,0,0]
	v_pk_mul_f32 v[218:219], v[32:33], v[32:33]
	v_pk_mul_f32 v[224:225], v[34:35], v[34:35]
	v_pk_mul_f32 v[230:231], v[40:41], v[40:41]
	v_pk_mul_f32 v[236:237], v[42:43], v[42:43]
	v_rcp_f32_e32 v214, v214
	v_rcp_f32_e32 v215, v215
	v_rcp_f32_e32 v220, v220
	v_rcp_f32_e32 v221, v221
	v_rcp_f32_e32 v226, v226
	v_rcp_f32_e32 v227, v227
	v_rcp_f32_e32 v232, v232
	v_rcp_f32_e32 v233, v233
	v_pk_mul_f32 v[218:219], v[218:219], s[68:69] op_sel_hi:[1,0]
	v_pk_mul_f32 v[224:225], v[224:225], s[68:69] op_sel_hi:[1,0]
	v_pk_mul_f32 v[230:231], v[230:231], s[68:69] op_sel_hi:[1,0]
	v_pk_mul_f32 v[236:237], v[236:237], s[68:69] op_sel_hi:[1,0]
	v_pk_fma_f32 v[216:217], v[214:215], s[58:59], v[238:239] op_sel_hi:[1,0,0]
	v_pk_fma_f32 v[222:223], v[220:221], s[58:59], v[238:239] op_sel_hi:[1,0,0]
	v_pk_fma_f32 v[228:229], v[226:227], s[58:59], v[238:239] op_sel_hi:[1,0,0]
	v_pk_fma_f32 v[234:235], v[232:233], s[58:59], v[238:239] op_sel_hi:[1,0,0]
	v_exp_f32_e32 v218, v218
	v_exp_f32_e32 v219, v219
	v_exp_f32_e32 v224, v224
	v_exp_f32_e32 v225, v225
	v_exp_f32_e32 v230, v230
	v_exp_f32_e32 v231, v231
	v_exp_f32_e32 v236, v236
	v_exp_f32_e32 v237, v237
	v_pk_fma_f32 v[216:217], v[214:215], v[216:217], s[62:63] op_sel_hi:[1,1,0]
	v_pk_fma_f32 v[222:223], v[220:221], v[222:223], s[62:63] op_sel_hi:[1,1,0]
	v_pk_fma_f32 v[228:229], v[226:227], v[228:229], s[62:63] op_sel_hi:[1,1,0]
	v_pk_fma_f32 v[234:235], v[232:233], v[234:235], s[62:63] op_sel_hi:[1,1,0]
	v_pk_fma_f32 v[216:217], v[214:215], v[216:217], s[64:65] op_sel_hi:[1,1,0]
	v_pk_fma_f32 v[222:223], v[220:221], v[222:223], s[64:65] op_sel_hi:[1,1,0]
	v_pk_fma_f32 v[228:229], v[226:227], v[228:229], s[64:65] op_sel_hi:[1,1,0]
	v_pk_fma_f32 v[234:235], v[232:233], v[234:235], s[64:65] op_sel_hi:[1,1,0]
	v_pk_fma_f32 v[216:217], v[214:215], v[216:217], s[66:67] op_sel_hi:[1,1,0]
	v_pk_fma_f32 v[222:223], v[220:221], v[222:223], s[66:67] op_sel_hi:[1,1,0]
	v_pk_fma_f32 v[228:229], v[226:227], v[228:229], s[66:67] op_sel_hi:[1,1,0]
	v_pk_fma_f32 v[234:235], v[232:233], v[234:235], s[66:67] op_sel_hi:[1,1,0]
	v_pk_mul_f32 v[216:217], v[214:215], v[216:217]
	v_pk_mul_f32 v[222:223], v[220:221], v[222:223]
	v_pk_mul_f32 v[228:229], v[226:227], v[228:229]
	v_pk_mul_f32 v[234:235], v[232:233], v[234:235]
	v_pk_mul_f32 v[216:217], v[218:219], v[216:217]
	v_pk_mul_f32 v[222:223], v[224:225], v[222:223]
	v_pk_mul_f32 v[228:229], v[230:231], v[228:229]
	v_pk_mul_f32 v[234:235], v[236:237], v[234:235]
	v_pk_mul_f32 v[214:215], v[32:33], v[216:217]
	v_pk_mul_f32 v[220:221], v[34:35], v[222:223]
	v_pk_mul_f32 v[226:227], v[40:41], v[228:229]
	v_pk_mul_f32 v[232:233], v[42:43], v[234:235]
	v_pk_fma_f32 v[218:219], v[32:33], v[216:217], v[32:33] neg_lo:[1,0,0] neg_hi:[1,0,0]
	v_pk_fma_f32 v[224:225], v[34:35], v[222:223], v[34:35] neg_lo:[1,0,0] neg_hi:[1,0,0]
	v_pk_fma_f32 v[230:231], v[40:41], v[228:229], v[40:41] neg_lo:[1,0,0] neg_hi:[1,0,0]
	v_pk_fma_f32 v[236:237], v[42:43], v[234:235], v[42:43] neg_lo:[1,0,0] neg_hi:[1,0,0]
	v_ashrrev_i32_e32 v216, 31, v32
	v_ashrrev_i32_e32 v217, 31, v33
	v_ashrrev_i32_e32 v222, 31, v34
	v_ashrrev_i32_e32 v223, 31, v35
	v_ashrrev_i32_e32 v228, 31, v40
	v_ashrrev_i32_e32 v229, 31, v41
	v_ashrrev_i32_e32 v234, 31, v42
	v_ashrrev_i32_e32 v235, 31, v43
	v_bfi_b32 v179, v216, v214, v218
	v_bfi_b32 v180, v217, v215, v219
	v_bfi_b32 v181, v222, v220, v224
	v_bfi_b32 v182, v223, v221, v225
	v_bfi_b32 v165, v228, v226, v230
	v_bfi_b32 v167, v229, v227, v231
	v_bfi_b32 v169, v234, v232, v236
	v_bfi_b32 v171, v235, v233, v237
.LBB0_265:
	s_nop 0
	v_cvt_pk_bf16_f32 v184, v165, v167
	v_cvt_pk_bf16_f32 v185, v169, v171
	v_cvt_pk_bf16_f32 v186, v179, v180
	v_cvt_pk_bf16_f32 v187, v181, v182
	s_and_b64 vcc, exec, s[6:7]
	v_mov_b32_e32 v179, v36
	v_mov_b32_e32 v180, v37
	v_mov_b32_e32 v181, v38
	v_mov_b32_e32 v182, v39
	v_mov_b32_e32 v165, v44
	v_mov_b32_e32 v167, v45
	v_mov_b32_e32 v169, v46
	v_mov_b32_e32 v171, v47
	global_store_dwordx4 v[174:175], v[184:187], off offset:16
	s_cbranch_vccnz .LBB0_267
	v_mov_b32_e32 v238, s60
	v_and_b32_e32 v214, 0x7fffffff, v36
	v_and_b32_e32 v215, 0x7fffffff, v37
	v_and_b32_e32 v220, 0x7fffffff, v38
	v_and_b32_e32 v221, 0x7fffffff, v39
	v_and_b32_e32 v226, 0x7fffffff, v44
	v_and_b32_e32 v227, 0x7fffffff, v45
	v_and_b32_e32 v232, 0x7fffffff, v46
	v_and_b32_e32 v233, 0x7fffffff, v47
	v_pk_fma_f32 v[214:215], v[214:215], s[56:57], 1.0 op_sel_hi:[1,0,0]
	v_pk_fma_f32 v[220:221], v[220:221], s[56:57], 1.0 op_sel_hi:[1,0,0]
	v_pk_fma_f32 v[226:227], v[226:227], s[56:57], 1.0 op_sel_hi:[1,0,0]
	v_pk_fma_f32 v[232:233], v[232:233], s[56:57], 1.0 op_sel_hi:[1,0,0]
	v_pk_mul_f32 v[218:219], v[36:37], v[36:37]
	v_pk_mul_f32 v[224:225], v[38:39], v[38:39]
	v_pk_mul_f32 v[230:231], v[44:45], v[44:45]
	v_pk_mul_f32 v[236:237], v[46:47], v[46:47]
	v_rcp_f32_e32 v214, v214
	v_rcp_f32_e32 v215, v215
	v_rcp_f32_e32 v220, v220
	v_rcp_f32_e32 v221, v221
	v_rcp_f32_e32 v226, v226
	v_rcp_f32_e32 v227, v227
	v_rcp_f32_e32 v232, v232
	v_rcp_f32_e32 v233, v233
	v_pk_mul_f32 v[218:219], v[218:219], s[68:69] op_sel_hi:[1,0]
	v_pk_mul_f32 v[224:225], v[224:225], s[68:69] op_sel_hi:[1,0]
	v_pk_mul_f32 v[230:231], v[230:231], s[68:69] op_sel_hi:[1,0]
	v_pk_mul_f32 v[236:237], v[236:237], s[68:69] op_sel_hi:[1,0]
	v_pk_fma_f32 v[216:217], v[214:215], s[58:59], v[238:239] op_sel_hi:[1,0,0]
	v_pk_fma_f32 v[222:223], v[220:221], s[58:59], v[238:239] op_sel_hi:[1,0,0]
	v_pk_fma_f32 v[228:229], v[226:227], s[58:59], v[238:239] op_sel_hi:[1,0,0]
	v_pk_fma_f32 v[234:235], v[232:233], s[58:59], v[238:239] op_sel_hi:[1,0,0]
	v_exp_f32_e32 v218, v218
	v_exp_f32_e32 v219, v219
	v_exp_f32_e32 v224, v224
	v_exp_f32_e32 v225, v225
	v_exp_f32_e32 v230, v230
	v_exp_f32_e32 v231, v231
	v_exp_f32_e32 v236, v236
	v_exp_f32_e32 v237, v237
	v_pk_fma_f32 v[216:217], v[214:215], v[216:217], s[62:63] op_sel_hi:[1,1,0]
	v_pk_fma_f32 v[222:223], v[220:221], v[222:223], s[62:63] op_sel_hi:[1,1,0]
	v_pk_fma_f32 v[228:229], v[226:227], v[228:229], s[62:63] op_sel_hi:[1,1,0]
	v_pk_fma_f32 v[234:235], v[232:233], v[234:235], s[62:63] op_sel_hi:[1,1,0]
	v_pk_fma_f32 v[216:217], v[214:215], v[216:217], s[64:65] op_sel_hi:[1,1,0]
	v_pk_fma_f32 v[222:223], v[220:221], v[222:223], s[64:65] op_sel_hi:[1,1,0]
	v_pk_fma_f32 v[228:229], v[226:227], v[228:229], s[64:65] op_sel_hi:[1,1,0]
	v_pk_fma_f32 v[234:235], v[232:233], v[234:235], s[64:65] op_sel_hi:[1,1,0]
	v_pk_fma_f32 v[216:217], v[214:215], v[216:217], s[66:67] op_sel_hi:[1,1,0]
	v_pk_fma_f32 v[222:223], v[220:221], v[222:223], s[66:67] op_sel_hi:[1,1,0]
	v_pk_fma_f32 v[228:229], v[226:227], v[228:229], s[66:67] op_sel_hi:[1,1,0]
	v_pk_fma_f32 v[234:235], v[232:233], v[234:235], s[66:67] op_sel_hi:[1,1,0]
	v_pk_mul_f32 v[216:217], v[214:215], v[216:217]
	v_pk_mul_f32 v[222:223], v[220:221], v[222:223]
	v_pk_mul_f32 v[228:229], v[226:227], v[228:229]
	v_pk_mul_f32 v[234:235], v[232:233], v[234:235]
	v_pk_mul_f32 v[216:217], v[218:219], v[216:217]
	v_pk_mul_f32 v[222:223], v[224:225], v[222:223]
	v_pk_mul_f32 v[228:229], v[230:231], v[228:229]
	v_pk_mul_f32 v[234:235], v[236:237], v[234:235]
	v_pk_mul_f32 v[214:215], v[36:37], v[216:217]
	v_pk_mul_f32 v[220:221], v[38:39], v[222:223]
	v_pk_mul_f32 v[226:227], v[44:45], v[228:229]
	v_pk_mul_f32 v[232:233], v[46:47], v[234:235]
	v_pk_fma_f32 v[218:219], v[36:37], v[216:217], v[36:37] neg_lo:[1,0,0] neg_hi:[1,0,0]
	v_pk_fma_f32 v[224:225], v[38:39], v[222:223], v[38:39] neg_lo:[1,0,0] neg_hi:[1,0,0]
	v_pk_fma_f32 v[230:231], v[44:45], v[228:229], v[44:45] neg_lo:[1,0,0] neg_hi:[1,0,0]
	v_pk_fma_f32 v[236:237], v[46:47], v[234:235], v[46:47] neg_lo:[1,0,0] neg_hi:[1,0,0]
	v_ashrrev_i32_e32 v216, 31, v36
	v_ashrrev_i32_e32 v217, 31, v37
	v_ashrrev_i32_e32 v222, 31, v38
	v_ashrrev_i32_e32 v223, 31, v39
	v_ashrrev_i32_e32 v228, 31, v44
	v_ashrrev_i32_e32 v229, 31, v45
	v_ashrrev_i32_e32 v234, 31, v46
	v_ashrrev_i32_e32 v235, 31, v47
	v_bfi_b32 v179, v216, v214, v218
	v_bfi_b32 v180, v217, v215, v219
	v_bfi_b32 v181, v222, v220, v224
	v_bfi_b32 v182, v223, v221, v225
	v_bfi_b32 v165, v228, v226, v230
	v_bfi_b32 v167, v229, v227, v231
	v_bfi_b32 v169, v234, v232, v236
	v_bfi_b32 v171, v235, v233, v237
.LBB0_267:
	v_add_u32_e32 v174, 0x80, v163
	v_mad_i64_i32 v[174:175], s[0:1], v174, s94, v[172:173]
	v_cvt_pk_bf16_f32 v184, v165, v167
	v_cvt_pk_bf16_f32 v185, v169, v171
	v_cvt_pk_bf16_f32 v186, v179, v180
	v_cvt_pk_bf16_f32 v187, v181, v182
	s_and_b64 vcc, exec, s[6:7]
	v_mov_b32_e32 v179, v0
	v_mov_b32_e32 v180, v1
	v_mov_b32_e32 v181, v2
	v_mov_b32_e32 v182, v3
	v_mov_b32_e32 v165, v4
	v_mov_b32_e32 v167, v5
	v_mov_b32_e32 v169, v6
	v_mov_b32_e32 v171, v7
	global_store_dwordx4 v[174:175], v[184:187], off
	s_cbranch_vccnz .LBB0_269
	v_mov_b32_e32 v238, s60
	v_and_b32_e32 v214, 0x7fffffff, v0
	v_and_b32_e32 v215, 0x7fffffff, v1
	v_and_b32_e32 v220, 0x7fffffff, v2
	v_and_b32_e32 v221, 0x7fffffff, v3
	v_and_b32_e32 v226, 0x7fffffff, v4
	v_and_b32_e32 v227, 0x7fffffff, v5
	v_and_b32_e32 v232, 0x7fffffff, v6
	v_and_b32_e32 v233, 0x7fffffff, v7
	v_pk_fma_f32 v[214:215], v[214:215], s[56:57], 1.0 op_sel_hi:[1,0,0]
	v_pk_fma_f32 v[220:221], v[220:221], s[56:57], 1.0 op_sel_hi:[1,0,0]
	v_pk_fma_f32 v[226:227], v[226:227], s[56:57], 1.0 op_sel_hi:[1,0,0]
	v_pk_fma_f32 v[232:233], v[232:233], s[56:57], 1.0 op_sel_hi:[1,0,0]
	v_pk_mul_f32 v[218:219], v[0:1], v[0:1]
	v_pk_mul_f32 v[224:225], v[2:3], v[2:3]
	v_pk_mul_f32 v[230:231], v[4:5], v[4:5]
	v_pk_mul_f32 v[236:237], v[6:7], v[6:7]
	v_rcp_f32_e32 v214, v214
	v_rcp_f32_e32 v215, v215
	v_rcp_f32_e32 v220, v220
	v_rcp_f32_e32 v221, v221
	v_rcp_f32_e32 v226, v226
	v_rcp_f32_e32 v227, v227
	v_rcp_f32_e32 v232, v232
	v_rcp_f32_e32 v233, v233
	v_pk_mul_f32 v[218:219], v[218:219], s[68:69] op_sel_hi:[1,0]
	v_pk_mul_f32 v[224:225], v[224:225], s[68:69] op_sel_hi:[1,0]
	v_pk_mul_f32 v[230:231], v[230:231], s[68:69] op_sel_hi:[1,0]
	v_pk_mul_f32 v[236:237], v[236:237], s[68:69] op_sel_hi:[1,0]
	v_pk_fma_f32 v[216:217], v[214:215], s[58:59], v[238:239] op_sel_hi:[1,0,0]
	v_pk_fma_f32 v[222:223], v[220:221], s[58:59], v[238:239] op_sel_hi:[1,0,0]
	v_pk_fma_f32 v[228:229], v[226:227], s[58:59], v[238:239] op_sel_hi:[1,0,0]
	v_pk_fma_f32 v[234:235], v[232:233], s[58:59], v[238:239] op_sel_hi:[1,0,0]
	v_exp_f32_e32 v218, v218
	v_exp_f32_e32 v219, v219
	v_exp_f32_e32 v224, v224
	v_exp_f32_e32 v225, v225
	v_exp_f32_e32 v230, v230
	v_exp_f32_e32 v231, v231
	v_exp_f32_e32 v236, v236
	v_exp_f32_e32 v237, v237
	v_pk_fma_f32 v[216:217], v[214:215], v[216:217], s[62:63] op_sel_hi:[1,1,0]
	v_pk_fma_f32 v[222:223], v[220:221], v[222:223], s[62:63] op_sel_hi:[1,1,0]
	v_pk_fma_f32 v[228:229], v[226:227], v[228:229], s[62:63] op_sel_hi:[1,1,0]
	v_pk_fma_f32 v[234:235], v[232:233], v[234:235], s[62:63] op_sel_hi:[1,1,0]
	v_pk_fma_f32 v[216:217], v[214:215], v[216:217], s[64:65] op_sel_hi:[1,1,0]
	v_pk_fma_f32 v[222:223], v[220:221], v[222:223], s[64:65] op_sel_hi:[1,1,0]
	v_pk_fma_f32 v[228:229], v[226:227], v[228:229], s[64:65] op_sel_hi:[1,1,0]
	v_pk_fma_f32 v[234:235], v[232:233], v[234:235], s[64:65] op_sel_hi:[1,1,0]
	v_pk_fma_f32 v[216:217], v[214:215], v[216:217], s[66:67] op_sel_hi:[1,1,0]
	v_pk_fma_f32 v[222:223], v[220:221], v[222:223], s[66:67] op_sel_hi:[1,1,0]
	v_pk_fma_f32 v[228:229], v[226:227], v[228:229], s[66:67] op_sel_hi:[1,1,0]
	v_pk_fma_f32 v[234:235], v[232:233], v[234:235], s[66:67] op_sel_hi:[1,1,0]
	v_pk_mul_f32 v[216:217], v[214:215], v[216:217]
	v_pk_mul_f32 v[222:223], v[220:221], v[222:223]
	v_pk_mul_f32 v[228:229], v[226:227], v[228:229]
	v_pk_mul_f32 v[234:235], v[232:233], v[234:235]
	v_pk_mul_f32 v[216:217], v[218:219], v[216:217]
	v_pk_mul_f32 v[222:223], v[224:225], v[222:223]
	v_pk_mul_f32 v[228:229], v[230:231], v[228:229]
	v_pk_mul_f32 v[234:235], v[236:237], v[234:235]
	v_pk_mul_f32 v[214:215], v[0:1], v[216:217]
	v_pk_mul_f32 v[220:221], v[2:3], v[222:223]
	v_pk_mul_f32 v[226:227], v[4:5], v[228:229]
	v_pk_mul_f32 v[232:233], v[6:7], v[234:235]
	v_pk_fma_f32 v[218:219], v[0:1], v[216:217], v[0:1] neg_lo:[1,0,0] neg_hi:[1,0,0]
	v_pk_fma_f32 v[224:225], v[2:3], v[222:223], v[2:3] neg_lo:[1,0,0] neg_hi:[1,0,0]
	v_pk_fma_f32 v[230:231], v[4:5], v[228:229], v[4:5] neg_lo:[1,0,0] neg_hi:[1,0,0]
	v_pk_fma_f32 v[236:237], v[6:7], v[234:235], v[6:7] neg_lo:[1,0,0] neg_hi:[1,0,0]
	v_ashrrev_i32_e32 v216, 31, v0
	v_ashrrev_i32_e32 v217, 31, v1
	v_ashrrev_i32_e32 v222, 31, v2
	v_ashrrev_i32_e32 v223, 31, v3
	v_ashrrev_i32_e32 v228, 31, v4
	v_ashrrev_i32_e32 v229, 31, v5
	v_ashrrev_i32_e32 v234, 31, v6
	v_ashrrev_i32_e32 v235, 31, v7
	v_bfi_b32 v179, v216, v214, v218
	v_bfi_b32 v180, v217, v215, v219
	v_bfi_b32 v181, v222, v220, v224
	v_bfi_b32 v182, v223, v221, v225
	v_bfi_b32 v165, v228, v226, v230
	v_bfi_b32 v167, v229, v227, v231
	v_bfi_b32 v169, v234, v232, v236
	v_bfi_b32 v171, v235, v233, v237
.LBB0_269:
	s_nop 0
	v_cvt_pk_bf16_f32 v184, v165, v167
	v_cvt_pk_bf16_f32 v185, v169, v171
	v_cvt_pk_bf16_f32 v186, v179, v180
	v_cvt_pk_bf16_f32 v187, v181, v182
	s_and_b64 vcc, exec, s[6:7]
	v_mov_b32_e32 v179, v24
	v_mov_b32_e32 v180, v25
	v_mov_b32_e32 v181, v26
	v_mov_b32_e32 v182, v27
	v_mov_b32_e32 v165, v28
	v_mov_b32_e32 v167, v29
	v_mov_b32_e32 v169, v30
	v_mov_b32_e32 v171, v31
	global_store_dwordx4 v[174:175], v[184:187], off offset:16
	s_cbranch_vccnz .LBB0_271
	v_mov_b32_e32 v238, s60
	v_and_b32_e32 v214, 0x7fffffff, v24
	v_and_b32_e32 v215, 0x7fffffff, v25
	v_and_b32_e32 v220, 0x7fffffff, v26
	v_and_b32_e32 v221, 0x7fffffff, v27
	v_and_b32_e32 v226, 0x7fffffff, v28
	v_and_b32_e32 v227, 0x7fffffff, v29
	v_and_b32_e32 v232, 0x7fffffff, v30
	v_and_b32_e32 v233, 0x7fffffff, v31
	v_pk_fma_f32 v[214:215], v[214:215], s[56:57], 1.0 op_sel_hi:[1,0,0]
	v_pk_fma_f32 v[220:221], v[220:221], s[56:57], 1.0 op_sel_hi:[1,0,0]
	v_pk_fma_f32 v[226:227], v[226:227], s[56:57], 1.0 op_sel_hi:[1,0,0]
	v_pk_fma_f32 v[232:233], v[232:233], s[56:57], 1.0 op_sel_hi:[1,0,0]
	v_pk_mul_f32 v[218:219], v[24:25], v[24:25]
	v_pk_mul_f32 v[224:225], v[26:27], v[26:27]
	v_pk_mul_f32 v[230:231], v[28:29], v[28:29]
	v_pk_mul_f32 v[236:237], v[30:31], v[30:31]
	v_rcp_f32_e32 v214, v214
	v_rcp_f32_e32 v215, v215
	v_rcp_f32_e32 v220, v220
	v_rcp_f32_e32 v221, v221
	v_rcp_f32_e32 v226, v226
	v_rcp_f32_e32 v227, v227
	v_rcp_f32_e32 v232, v232
	v_rcp_f32_e32 v233, v233
	v_pk_mul_f32 v[218:219], v[218:219], s[68:69] op_sel_hi:[1,0]
	v_pk_mul_f32 v[224:225], v[224:225], s[68:69] op_sel_hi:[1,0]
	v_pk_mul_f32 v[230:231], v[230:231], s[68:69] op_sel_hi:[1,0]
	v_pk_mul_f32 v[236:237], v[236:237], s[68:69] op_sel_hi:[1,0]
	v_pk_fma_f32 v[216:217], v[214:215], s[58:59], v[238:239] op_sel_hi:[1,0,0]
	v_pk_fma_f32 v[222:223], v[220:221], s[58:59], v[238:239] op_sel_hi:[1,0,0]
	v_pk_fma_f32 v[228:229], v[226:227], s[58:59], v[238:239] op_sel_hi:[1,0,0]
	v_pk_fma_f32 v[234:235], v[232:233], s[58:59], v[238:239] op_sel_hi:[1,0,0]
	v_exp_f32_e32 v218, v218
	v_exp_f32_e32 v219, v219
	v_exp_f32_e32 v224, v224
	v_exp_f32_e32 v225, v225
	v_exp_f32_e32 v230, v230
	v_exp_f32_e32 v231, v231
	v_exp_f32_e32 v236, v236
	v_exp_f32_e32 v237, v237
	v_pk_fma_f32 v[216:217], v[214:215], v[216:217], s[62:63] op_sel_hi:[1,1,0]
	v_pk_fma_f32 v[222:223], v[220:221], v[222:223], s[62:63] op_sel_hi:[1,1,0]
	v_pk_fma_f32 v[228:229], v[226:227], v[228:229], s[62:63] op_sel_hi:[1,1,0]
	v_pk_fma_f32 v[234:235], v[232:233], v[234:235], s[62:63] op_sel_hi:[1,1,0]
	v_pk_fma_f32 v[216:217], v[214:215], v[216:217], s[64:65] op_sel_hi:[1,1,0]
	v_pk_fma_f32 v[222:223], v[220:221], v[222:223], s[64:65] op_sel_hi:[1,1,0]
	v_pk_fma_f32 v[228:229], v[226:227], v[228:229], s[64:65] op_sel_hi:[1,1,0]
	v_pk_fma_f32 v[234:235], v[232:233], v[234:235], s[64:65] op_sel_hi:[1,1,0]
	v_pk_fma_f32 v[216:217], v[214:215], v[216:217], s[66:67] op_sel_hi:[1,1,0]
	v_pk_fma_f32 v[222:223], v[220:221], v[222:223], s[66:67] op_sel_hi:[1,1,0]
	v_pk_fma_f32 v[228:229], v[226:227], v[228:229], s[66:67] op_sel_hi:[1,1,0]
	v_pk_fma_f32 v[234:235], v[232:233], v[234:235], s[66:67] op_sel_hi:[1,1,0]
	v_pk_mul_f32 v[216:217], v[214:215], v[216:217]
	v_pk_mul_f32 v[222:223], v[220:221], v[222:223]
	v_pk_mul_f32 v[228:229], v[226:227], v[228:229]
	v_pk_mul_f32 v[234:235], v[232:233], v[234:235]
	v_pk_mul_f32 v[216:217], v[218:219], v[216:217]
	v_pk_mul_f32 v[222:223], v[224:225], v[222:223]
	v_pk_mul_f32 v[228:229], v[230:231], v[228:229]
	v_pk_mul_f32 v[234:235], v[236:237], v[234:235]
	v_pk_mul_f32 v[214:215], v[24:25], v[216:217]
	v_pk_mul_f32 v[220:221], v[26:27], v[222:223]
	v_pk_mul_f32 v[226:227], v[28:29], v[228:229]
	v_pk_mul_f32 v[232:233], v[30:31], v[234:235]
	v_pk_fma_f32 v[218:219], v[24:25], v[216:217], v[24:25] neg_lo:[1,0,0] neg_hi:[1,0,0]
	v_pk_fma_f32 v[224:225], v[26:27], v[222:223], v[26:27] neg_lo:[1,0,0] neg_hi:[1,0,0]
	v_pk_fma_f32 v[230:231], v[28:29], v[228:229], v[28:29] neg_lo:[1,0,0] neg_hi:[1,0,0]
	v_pk_fma_f32 v[236:237], v[30:31], v[234:235], v[30:31] neg_lo:[1,0,0] neg_hi:[1,0,0]
	v_ashrrev_i32_e32 v216, 31, v24
	v_ashrrev_i32_e32 v217, 31, v25
	v_ashrrev_i32_e32 v222, 31, v26
	v_ashrrev_i32_e32 v223, 31, v27
	v_ashrrev_i32_e32 v228, 31, v28
	v_ashrrev_i32_e32 v229, 31, v29
	v_ashrrev_i32_e32 v234, 31, v30
	v_ashrrev_i32_e32 v235, 31, v31
	v_bfi_b32 v179, v216, v214, v218
	v_bfi_b32 v180, v217, v215, v219
	v_bfi_b32 v181, v222, v220, v224
	v_bfi_b32 v182, v223, v221, v225
	v_bfi_b32 v165, v228, v226, v230
	v_bfi_b32 v167, v229, v227, v231
	v_bfi_b32 v169, v234, v232, v236
	v_bfi_b32 v171, v235, v233, v237
.LBB0_271:
	v_add_u32_e32 v174, 0x90, v163
	v_mad_i64_i32 v[174:175], s[0:1], v174, s94, v[172:173]
	v_cvt_pk_bf16_f32 v184, v165, v167
	v_cvt_pk_bf16_f32 v185, v169, v171
	v_cvt_pk_bf16_f32 v186, v179, v180
	v_cvt_pk_bf16_f32 v187, v181, v182
	s_and_b64 vcc, exec, s[6:7]
	v_mov_b32_e32 v179, v108
	v_mov_b32_e32 v180, v109
	v_mov_b32_e32 v181, v110
	v_mov_b32_e32 v182, v111
	v_mov_b32_e32 v165, v104
	v_mov_b32_e32 v167, v105
	v_mov_b32_e32 v169, v106
	v_mov_b32_e32 v171, v107
	global_store_dwordx4 v[174:175], v[184:187], off
	s_cbranch_vccnz .LBB0_273
	v_mov_b32_e32 v238, s60
	v_and_b32_e32 v214, 0x7fffffff, v104
	v_and_b32_e32 v215, 0x7fffffff, v105
	v_and_b32_e32 v220, 0x7fffffff, v106
	v_and_b32_e32 v221, 0x7fffffff, v107
	v_and_b32_e32 v226, 0x7fffffff, v108
	v_and_b32_e32 v227, 0x7fffffff, v109
	v_and_b32_e32 v232, 0x7fffffff, v110
	v_and_b32_e32 v233, 0x7fffffff, v111
	v_pk_fma_f32 v[214:215], v[214:215], s[56:57], 1.0 op_sel_hi:[1,0,0]
	v_pk_fma_f32 v[220:221], v[220:221], s[56:57], 1.0 op_sel_hi:[1,0,0]
	v_pk_fma_f32 v[226:227], v[226:227], s[56:57], 1.0 op_sel_hi:[1,0,0]
	v_pk_fma_f32 v[232:233], v[232:233], s[56:57], 1.0 op_sel_hi:[1,0,0]
	v_pk_mul_f32 v[218:219], v[104:105], v[104:105]
	v_pk_mul_f32 v[224:225], v[106:107], v[106:107]
	v_pk_mul_f32 v[230:231], v[108:109], v[108:109]
	v_pk_mul_f32 v[236:237], v[110:111], v[110:111]
	v_rcp_f32_e32 v214, v214
	v_rcp_f32_e32 v215, v215
	v_rcp_f32_e32 v220, v220
	v_rcp_f32_e32 v221, v221
	v_rcp_f32_e32 v226, v226
	v_rcp_f32_e32 v227, v227
	v_rcp_f32_e32 v232, v232
	v_rcp_f32_e32 v233, v233
	v_pk_mul_f32 v[218:219], v[218:219], s[68:69] op_sel_hi:[1,0]
	v_pk_mul_f32 v[224:225], v[224:225], s[68:69] op_sel_hi:[1,0]
	v_pk_mul_f32 v[230:231], v[230:231], s[68:69] op_sel_hi:[1,0]
	v_pk_mul_f32 v[236:237], v[236:237], s[68:69] op_sel_hi:[1,0]
	v_pk_fma_f32 v[216:217], v[214:215], s[58:59], v[238:239] op_sel_hi:[1,0,0]
	v_pk_fma_f32 v[222:223], v[220:221], s[58:59], v[238:239] op_sel_hi:[1,0,0]
	v_pk_fma_f32 v[228:229], v[226:227], s[58:59], v[238:239] op_sel_hi:[1,0,0]
	v_pk_fma_f32 v[234:235], v[232:233], s[58:59], v[238:239] op_sel_hi:[1,0,0]
	v_exp_f32_e32 v218, v218
	v_exp_f32_e32 v219, v219
	v_exp_f32_e32 v224, v224
	v_exp_f32_e32 v225, v225
	v_exp_f32_e32 v230, v230
	v_exp_f32_e32 v231, v231
	v_exp_f32_e32 v236, v236
	v_exp_f32_e32 v237, v237
	v_pk_fma_f32 v[216:217], v[214:215], v[216:217], s[62:63] op_sel_hi:[1,1,0]
	v_pk_fma_f32 v[222:223], v[220:221], v[222:223], s[62:63] op_sel_hi:[1,1,0]
	v_pk_fma_f32 v[228:229], v[226:227], v[228:229], s[62:63] op_sel_hi:[1,1,0]
	v_pk_fma_f32 v[234:235], v[232:233], v[234:235], s[62:63] op_sel_hi:[1,1,0]
	v_pk_fma_f32 v[216:217], v[214:215], v[216:217], s[64:65] op_sel_hi:[1,1,0]
	v_pk_fma_f32 v[222:223], v[220:221], v[222:223], s[64:65] op_sel_hi:[1,1,0]
	v_pk_fma_f32 v[228:229], v[226:227], v[228:229], s[64:65] op_sel_hi:[1,1,0]
	v_pk_fma_f32 v[234:235], v[232:233], v[234:235], s[64:65] op_sel_hi:[1,1,0]
	v_pk_fma_f32 v[216:217], v[214:215], v[216:217], s[66:67] op_sel_hi:[1,1,0]
	v_pk_fma_f32 v[222:223], v[220:221], v[222:223], s[66:67] op_sel_hi:[1,1,0]
	v_pk_fma_f32 v[228:229], v[226:227], v[228:229], s[66:67] op_sel_hi:[1,1,0]
	v_pk_fma_f32 v[234:235], v[232:233], v[234:235], s[66:67] op_sel_hi:[1,1,0]
	v_pk_mul_f32 v[216:217], v[214:215], v[216:217]
	v_pk_mul_f32 v[222:223], v[220:221], v[222:223]
	v_pk_mul_f32 v[228:229], v[226:227], v[228:229]
	v_pk_mul_f32 v[234:235], v[232:233], v[234:235]
	v_pk_mul_f32 v[216:217], v[218:219], v[216:217]
	v_pk_mul_f32 v[222:223], v[224:225], v[222:223]
	v_pk_mul_f32 v[228:229], v[230:231], v[228:229]
	v_pk_mul_f32 v[234:235], v[236:237], v[234:235]
	v_pk_mul_f32 v[214:215], v[104:105], v[216:217]
	v_pk_mul_f32 v[220:221], v[106:107], v[222:223]
	v_pk_mul_f32 v[226:227], v[108:109], v[228:229]
	v_pk_mul_f32 v[232:233], v[110:111], v[234:235]
	v_pk_fma_f32 v[218:219], v[104:105], v[216:217], v[104:105] neg_lo:[1,0,0] neg_hi:[1,0,0]
	v_pk_fma_f32 v[224:225], v[106:107], v[222:223], v[106:107] neg_lo:[1,0,0] neg_hi:[1,0,0]
	v_pk_fma_f32 v[230:231], v[108:109], v[228:229], v[108:109] neg_lo:[1,0,0] neg_hi:[1,0,0]
	v_pk_fma_f32 v[236:237], v[110:111], v[234:235], v[110:111] neg_lo:[1,0,0] neg_hi:[1,0,0]
	v_ashrrev_i32_e32 v216, 31, v104
	v_ashrrev_i32_e32 v217, 31, v105
	v_ashrrev_i32_e32 v222, 31, v106
	v_ashrrev_i32_e32 v223, 31, v107
	v_ashrrev_i32_e32 v228, 31, v108
	v_ashrrev_i32_e32 v229, 31, v109
	v_ashrrev_i32_e32 v234, 31, v110
	v_ashrrev_i32_e32 v235, 31, v111
	v_bfi_b32 v165, v216, v214, v218
	v_bfi_b32 v167, v217, v215, v219
	v_bfi_b32 v169, v222, v220, v224
	v_bfi_b32 v171, v223, v221, v225
	v_bfi_b32 v179, v228, v226, v230
	v_bfi_b32 v180, v229, v227, v231
	v_bfi_b32 v181, v234, v232, v236
	v_bfi_b32 v182, v235, v233, v237
.LBB0_273:
	s_nop 0
	v_cvt_pk_bf16_f32 v184, v165, v167
	v_cvt_pk_bf16_f32 v185, v169, v171
	v_cvt_pk_bf16_f32 v186, v179, v180
	v_cvt_pk_bf16_f32 v187, v181, v182
	s_and_b64 vcc, exec, s[6:7]
	v_mov_b32_e32 v179, v16
	v_mov_b32_e32 v180, v17
	v_mov_b32_e32 v181, v18
	v_mov_b32_e32 v182, v19
	v_mov_b32_e32 v165, v20
	v_mov_b32_e32 v167, v21
	v_mov_b32_e32 v169, v22
	v_mov_b32_e32 v171, v23
	global_store_dwordx4 v[174:175], v[184:187], off offset:16
	s_cbranch_vccnz .LBB0_275
	v_mov_b32_e32 v238, s60
	v_and_b32_e32 v214, 0x7fffffff, v16
	v_and_b32_e32 v215, 0x7fffffff, v17
	v_and_b32_e32 v220, 0x7fffffff, v18
	v_and_b32_e32 v221, 0x7fffffff, v19
	v_and_b32_e32 v226, 0x7fffffff, v20
	v_and_b32_e32 v227, 0x7fffffff, v21
	v_and_b32_e32 v232, 0x7fffffff, v22
	v_and_b32_e32 v233, 0x7fffffff, v23
	v_pk_fma_f32 v[214:215], v[214:215], s[56:57], 1.0 op_sel_hi:[1,0,0]
	v_pk_fma_f32 v[220:221], v[220:221], s[56:57], 1.0 op_sel_hi:[1,0,0]
	v_pk_fma_f32 v[226:227], v[226:227], s[56:57], 1.0 op_sel_hi:[1,0,0]
	v_pk_fma_f32 v[232:233], v[232:233], s[56:57], 1.0 op_sel_hi:[1,0,0]
	v_pk_mul_f32 v[218:219], v[16:17], v[16:17]
	v_pk_mul_f32 v[224:225], v[18:19], v[18:19]
	v_pk_mul_f32 v[230:231], v[20:21], v[20:21]
	v_pk_mul_f32 v[236:237], v[22:23], v[22:23]
	v_rcp_f32_e32 v214, v214
	v_rcp_f32_e32 v215, v215
	v_rcp_f32_e32 v220, v220
	v_rcp_f32_e32 v221, v221
	v_rcp_f32_e32 v226, v226
	v_rcp_f32_e32 v227, v227
	v_rcp_f32_e32 v232, v232
	v_rcp_f32_e32 v233, v233
	v_pk_mul_f32 v[218:219], v[218:219], s[68:69] op_sel_hi:[1,0]
	v_pk_mul_f32 v[224:225], v[224:225], s[68:69] op_sel_hi:[1,0]
	v_pk_mul_f32 v[230:231], v[230:231], s[68:69] op_sel_hi:[1,0]
	v_pk_mul_f32 v[236:237], v[236:237], s[68:69] op_sel_hi:[1,0]
	v_pk_fma_f32 v[216:217], v[214:215], s[58:59], v[238:239] op_sel_hi:[1,0,0]
	v_pk_fma_f32 v[222:223], v[220:221], s[58:59], v[238:239] op_sel_hi:[1,0,0]
	v_pk_fma_f32 v[228:229], v[226:227], s[58:59], v[238:239] op_sel_hi:[1,0,0]
	v_pk_fma_f32 v[234:235], v[232:233], s[58:59], v[238:239] op_sel_hi:[1,0,0]
	v_exp_f32_e32 v218, v218
	v_exp_f32_e32 v219, v219
	v_exp_f32_e32 v224, v224
	v_exp_f32_e32 v225, v225
	v_exp_f32_e32 v230, v230
	v_exp_f32_e32 v231, v231
	v_exp_f32_e32 v236, v236
	v_exp_f32_e32 v237, v237
	v_pk_fma_f32 v[216:217], v[214:215], v[216:217], s[62:63] op_sel_hi:[1,1,0]
	v_pk_fma_f32 v[222:223], v[220:221], v[222:223], s[62:63] op_sel_hi:[1,1,0]
	v_pk_fma_f32 v[228:229], v[226:227], v[228:229], s[62:63] op_sel_hi:[1,1,0]
	v_pk_fma_f32 v[234:235], v[232:233], v[234:235], s[62:63] op_sel_hi:[1,1,0]
	v_pk_fma_f32 v[216:217], v[214:215], v[216:217], s[64:65] op_sel_hi:[1,1,0]
	v_pk_fma_f32 v[222:223], v[220:221], v[222:223], s[64:65] op_sel_hi:[1,1,0]
	v_pk_fma_f32 v[228:229], v[226:227], v[228:229], s[64:65] op_sel_hi:[1,1,0]
	v_pk_fma_f32 v[234:235], v[232:233], v[234:235], s[64:65] op_sel_hi:[1,1,0]
	v_pk_fma_f32 v[216:217], v[214:215], v[216:217], s[66:67] op_sel_hi:[1,1,0]
	v_pk_fma_f32 v[222:223], v[220:221], v[222:223], s[66:67] op_sel_hi:[1,1,0]
	v_pk_fma_f32 v[228:229], v[226:227], v[228:229], s[66:67] op_sel_hi:[1,1,0]
	v_pk_fma_f32 v[234:235], v[232:233], v[234:235], s[66:67] op_sel_hi:[1,1,0]
	v_pk_mul_f32 v[216:217], v[214:215], v[216:217]
	v_pk_mul_f32 v[222:223], v[220:221], v[222:223]
	v_pk_mul_f32 v[228:229], v[226:227], v[228:229]
	v_pk_mul_f32 v[234:235], v[232:233], v[234:235]
	v_pk_mul_f32 v[216:217], v[218:219], v[216:217]
	v_pk_mul_f32 v[222:223], v[224:225], v[222:223]
	v_pk_mul_f32 v[228:229], v[230:231], v[228:229]
	v_pk_mul_f32 v[234:235], v[236:237], v[234:235]
	v_pk_mul_f32 v[214:215], v[16:17], v[216:217]
	v_pk_mul_f32 v[220:221], v[18:19], v[222:223]
	v_pk_mul_f32 v[226:227], v[20:21], v[228:229]
	v_pk_mul_f32 v[232:233], v[22:23], v[234:235]
	v_pk_fma_f32 v[218:219], v[16:17], v[216:217], v[16:17] neg_lo:[1,0,0] neg_hi:[1,0,0]
	v_pk_fma_f32 v[224:225], v[18:19], v[222:223], v[18:19] neg_lo:[1,0,0] neg_hi:[1,0,0]
	v_pk_fma_f32 v[230:231], v[20:21], v[228:229], v[20:21] neg_lo:[1,0,0] neg_hi:[1,0,0]
	v_pk_fma_f32 v[236:237], v[22:23], v[234:235], v[22:23] neg_lo:[1,0,0] neg_hi:[1,0,0]
	v_ashrrev_i32_e32 v216, 31, v16
	v_ashrrev_i32_e32 v217, 31, v17
	v_ashrrev_i32_e32 v222, 31, v18
	v_ashrrev_i32_e32 v223, 31, v19
	v_ashrrev_i32_e32 v228, 31, v20
	v_ashrrev_i32_e32 v229, 31, v21
	v_ashrrev_i32_e32 v234, 31, v22
	v_ashrrev_i32_e32 v235, 31, v23
	v_bfi_b32 v179, v216, v214, v218
	v_bfi_b32 v180, v217, v215, v219
	v_bfi_b32 v181, v222, v220, v224
	v_bfi_b32 v182, v223, v221, v225
	v_bfi_b32 v165, v228, v226, v230
	v_bfi_b32 v167, v229, v227, v231
	v_bfi_b32 v169, v234, v232, v236
	v_bfi_b32 v171, v235, v233, v237
.LBB0_275:
	v_add_u32_e32 v174, 0xa0, v163
	v_mad_i64_i32 v[174:175], s[0:1], v174, s94, v[172:173]
	v_cvt_pk_bf16_f32 v184, v165, v167
	v_cvt_pk_bf16_f32 v185, v169, v171
	v_cvt_pk_bf16_f32 v186, v179, v180
	v_cvt_pk_bf16_f32 v187, v181, v182
	s_and_b64 vcc, exec, s[6:7]
	v_mov_b32_e32 v179, v116
	v_mov_b32_e32 v180, v117
	v_mov_b32_e32 v181, v118
	v_mov_b32_e32 v182, v119
	v_mov_b32_e32 v165, v112
	v_mov_b32_e32 v167, v113
	v_mov_b32_e32 v169, v114
	v_mov_b32_e32 v171, v115
	global_store_dwordx4 v[174:175], v[184:187], off
	s_cbranch_vccnz .LBB0_277
	v_mov_b32_e32 v238, s60
	v_and_b32_e32 v214, 0x7fffffff, v112
	v_and_b32_e32 v215, 0x7fffffff, v113
	v_and_b32_e32 v220, 0x7fffffff, v114
	v_and_b32_e32 v221, 0x7fffffff, v115
	v_and_b32_e32 v226, 0x7fffffff, v116
	v_and_b32_e32 v227, 0x7fffffff, v117
	v_and_b32_e32 v232, 0x7fffffff, v118
	v_and_b32_e32 v233, 0x7fffffff, v119
	v_pk_fma_f32 v[214:215], v[214:215], s[56:57], 1.0 op_sel_hi:[1,0,0]
	v_pk_fma_f32 v[220:221], v[220:221], s[56:57], 1.0 op_sel_hi:[1,0,0]
	v_pk_fma_f32 v[226:227], v[226:227], s[56:57], 1.0 op_sel_hi:[1,0,0]
	v_pk_fma_f32 v[232:233], v[232:233], s[56:57], 1.0 op_sel_hi:[1,0,0]
	v_pk_mul_f32 v[218:219], v[112:113], v[112:113]
	v_pk_mul_f32 v[224:225], v[114:115], v[114:115]
	v_pk_mul_f32 v[230:231], v[116:117], v[116:117]
	v_pk_mul_f32 v[236:237], v[118:119], v[118:119]
	v_rcp_f32_e32 v214, v214
	v_rcp_f32_e32 v215, v215
	v_rcp_f32_e32 v220, v220
	v_rcp_f32_e32 v221, v221
	v_rcp_f32_e32 v226, v226
	v_rcp_f32_e32 v227, v227
	v_rcp_f32_e32 v232, v232
	v_rcp_f32_e32 v233, v233
	v_pk_mul_f32 v[218:219], v[218:219], s[68:69] op_sel_hi:[1,0]
	v_pk_mul_f32 v[224:225], v[224:225], s[68:69] op_sel_hi:[1,0]
	v_pk_mul_f32 v[230:231], v[230:231], s[68:69] op_sel_hi:[1,0]
	v_pk_mul_f32 v[236:237], v[236:237], s[68:69] op_sel_hi:[1,0]
	v_pk_fma_f32 v[216:217], v[214:215], s[58:59], v[238:239] op_sel_hi:[1,0,0]
	v_pk_fma_f32 v[222:223], v[220:221], s[58:59], v[238:239] op_sel_hi:[1,0,0]
	v_pk_fma_f32 v[228:229], v[226:227], s[58:59], v[238:239] op_sel_hi:[1,0,0]
	v_pk_fma_f32 v[234:235], v[232:233], s[58:59], v[238:239] op_sel_hi:[1,0,0]
	v_exp_f32_e32 v218, v218
	v_exp_f32_e32 v219, v219
	v_exp_f32_e32 v224, v224
	v_exp_f32_e32 v225, v225
	v_exp_f32_e32 v230, v230
	v_exp_f32_e32 v231, v231
	v_exp_f32_e32 v236, v236
	v_exp_f32_e32 v237, v237
	v_pk_fma_f32 v[216:217], v[214:215], v[216:217], s[62:63] op_sel_hi:[1,1,0]
	v_pk_fma_f32 v[222:223], v[220:221], v[222:223], s[62:63] op_sel_hi:[1,1,0]
	v_pk_fma_f32 v[228:229], v[226:227], v[228:229], s[62:63] op_sel_hi:[1,1,0]
	v_pk_fma_f32 v[234:235], v[232:233], v[234:235], s[62:63] op_sel_hi:[1,1,0]
	v_pk_fma_f32 v[216:217], v[214:215], v[216:217], s[64:65] op_sel_hi:[1,1,0]
	v_pk_fma_f32 v[222:223], v[220:221], v[222:223], s[64:65] op_sel_hi:[1,1,0]
	v_pk_fma_f32 v[228:229], v[226:227], v[228:229], s[64:65] op_sel_hi:[1,1,0]
	v_pk_fma_f32 v[234:235], v[232:233], v[234:235], s[64:65] op_sel_hi:[1,1,0]
	v_pk_fma_f32 v[216:217], v[214:215], v[216:217], s[66:67] op_sel_hi:[1,1,0]
	v_pk_fma_f32 v[222:223], v[220:221], v[222:223], s[66:67] op_sel_hi:[1,1,0]
	v_pk_fma_f32 v[228:229], v[226:227], v[228:229], s[66:67] op_sel_hi:[1,1,0]
	v_pk_fma_f32 v[234:235], v[232:233], v[234:235], s[66:67] op_sel_hi:[1,1,0]
	v_pk_mul_f32 v[216:217], v[214:215], v[216:217]
	v_pk_mul_f32 v[222:223], v[220:221], v[222:223]
	v_pk_mul_f32 v[228:229], v[226:227], v[228:229]
	v_pk_mul_f32 v[234:235], v[232:233], v[234:235]
	v_pk_mul_f32 v[216:217], v[218:219], v[216:217]
	v_pk_mul_f32 v[222:223], v[224:225], v[222:223]
	v_pk_mul_f32 v[228:229], v[230:231], v[228:229]
	v_pk_mul_f32 v[234:235], v[236:237], v[234:235]
	v_pk_mul_f32 v[214:215], v[112:113], v[216:217]
	v_pk_mul_f32 v[220:221], v[114:115], v[222:223]
	v_pk_mul_f32 v[226:227], v[116:117], v[228:229]
	v_pk_mul_f32 v[232:233], v[118:119], v[234:235]
	v_pk_fma_f32 v[218:219], v[112:113], v[216:217], v[112:113] neg_lo:[1,0,0] neg_hi:[1,0,0]
	v_pk_fma_f32 v[224:225], v[114:115], v[222:223], v[114:115] neg_lo:[1,0,0] neg_hi:[1,0,0]
	v_pk_fma_f32 v[230:231], v[116:117], v[228:229], v[116:117] neg_lo:[1,0,0] neg_hi:[1,0,0]
	v_pk_fma_f32 v[236:237], v[118:119], v[234:235], v[118:119] neg_lo:[1,0,0] neg_hi:[1,0,0]
	v_ashrrev_i32_e32 v216, 31, v112
	v_ashrrev_i32_e32 v217, 31, v113
	v_ashrrev_i32_e32 v222, 31, v114
	v_ashrrev_i32_e32 v223, 31, v115
	v_ashrrev_i32_e32 v228, 31, v116
	v_ashrrev_i32_e32 v229, 31, v117
	v_ashrrev_i32_e32 v234, 31, v118
	v_ashrrev_i32_e32 v235, 31, v119
	v_bfi_b32 v165, v216, v214, v218
	v_bfi_b32 v167, v217, v215, v219
	v_bfi_b32 v169, v222, v220, v224
	v_bfi_b32 v171, v223, v221, v225
	v_bfi_b32 v179, v228, v226, v230
	v_bfi_b32 v180, v229, v227, v231
	v_bfi_b32 v181, v234, v232, v236
	v_bfi_b32 v182, v235, v233, v237
.LBB0_277:
	s_nop 0
	v_cvt_pk_bf16_f32 v184, v165, v167
	v_cvt_pk_bf16_f32 v185, v169, v171
	v_cvt_pk_bf16_f32 v186, v179, v180
	v_cvt_pk_bf16_f32 v187, v181, v182
	global_store_dwordx4 v[174:175], v[184:187], off offset:16
	s_and_b64 vcc, exec, s[6:7]
	v_mov_b32_e32 v174, v8
	v_mov_b32_e32 v175, v9
	v_mov_b32_e32 v179, v10
	v_mov_b32_e32 v180, v11
	v_mov_b32_e32 v165, v12
	v_mov_b32_e32 v167, v13
	v_mov_b32_e32 v169, v14
	v_mov_b32_e32 v171, v15
	s_cbranch_vccnz .LBB0_279
	v_mov_b32_e32 v238, s60
	v_and_b32_e32 v214, 0x7fffffff, v8
	v_and_b32_e32 v215, 0x7fffffff, v9
	v_and_b32_e32 v220, 0x7fffffff, v10
	v_and_b32_e32 v221, 0x7fffffff, v11
	v_and_b32_e32 v226, 0x7fffffff, v12
	v_and_b32_e32 v227, 0x7fffffff, v13
	v_and_b32_e32 v232, 0x7fffffff, v14
	v_and_b32_e32 v233, 0x7fffffff, v15
	v_pk_fma_f32 v[214:215], v[214:215], s[56:57], 1.0 op_sel_hi:[1,0,0]
	v_pk_fma_f32 v[220:221], v[220:221], s[56:57], 1.0 op_sel_hi:[1,0,0]
	v_pk_fma_f32 v[226:227], v[226:227], s[56:57], 1.0 op_sel_hi:[1,0,0]
	v_pk_fma_f32 v[232:233], v[232:233], s[56:57], 1.0 op_sel_hi:[1,0,0]
	v_pk_mul_f32 v[218:219], v[8:9], v[8:9]
	v_pk_mul_f32 v[224:225], v[10:11], v[10:11]
	v_pk_mul_f32 v[230:231], v[12:13], v[12:13]
	v_pk_mul_f32 v[236:237], v[14:15], v[14:15]
	v_rcp_f32_e32 v214, v214
	v_rcp_f32_e32 v215, v215
	v_rcp_f32_e32 v220, v220
	v_rcp_f32_e32 v221, v221
	v_rcp_f32_e32 v226, v226
	v_rcp_f32_e32 v227, v227
	v_rcp_f32_e32 v232, v232
	v_rcp_f32_e32 v233, v233
	v_pk_mul_f32 v[218:219], v[218:219], s[68:69] op_sel_hi:[1,0]
	v_pk_mul_f32 v[224:225], v[224:225], s[68:69] op_sel_hi:[1,0]
	v_pk_mul_f32 v[230:231], v[230:231], s[68:69] op_sel_hi:[1,0]
	v_pk_mul_f32 v[236:237], v[236:237], s[68:69] op_sel_hi:[1,0]
	v_pk_fma_f32 v[216:217], v[214:215], s[58:59], v[238:239] op_sel_hi:[1,0,0]
	v_pk_fma_f32 v[222:223], v[220:221], s[58:59], v[238:239] op_sel_hi:[1,0,0]
	v_pk_fma_f32 v[228:229], v[226:227], s[58:59], v[238:239] op_sel_hi:[1,0,0]
	v_pk_fma_f32 v[234:235], v[232:233], s[58:59], v[238:239] op_sel_hi:[1,0,0]
	v_exp_f32_e32 v218, v218
	v_exp_f32_e32 v219, v219
	v_exp_f32_e32 v224, v224
	v_exp_f32_e32 v225, v225
	v_exp_f32_e32 v230, v230
	v_exp_f32_e32 v231, v231
	v_exp_f32_e32 v236, v236
	v_exp_f32_e32 v237, v237
	v_pk_fma_f32 v[216:217], v[214:215], v[216:217], s[62:63] op_sel_hi:[1,1,0]
	v_pk_fma_f32 v[222:223], v[220:221], v[222:223], s[62:63] op_sel_hi:[1,1,0]
	v_pk_fma_f32 v[228:229], v[226:227], v[228:229], s[62:63] op_sel_hi:[1,1,0]
	v_pk_fma_f32 v[234:235], v[232:233], v[234:235], s[62:63] op_sel_hi:[1,1,0]
	v_pk_fma_f32 v[216:217], v[214:215], v[216:217], s[64:65] op_sel_hi:[1,1,0]
	v_pk_fma_f32 v[222:223], v[220:221], v[222:223], s[64:65] op_sel_hi:[1,1,0]
	v_pk_fma_f32 v[228:229], v[226:227], v[228:229], s[64:65] op_sel_hi:[1,1,0]
	v_pk_fma_f32 v[234:235], v[232:233], v[234:235], s[64:65] op_sel_hi:[1,1,0]
	v_pk_fma_f32 v[216:217], v[214:215], v[216:217], s[66:67] op_sel_hi:[1,1,0]
	v_pk_fma_f32 v[222:223], v[220:221], v[222:223], s[66:67] op_sel_hi:[1,1,0]
	v_pk_fma_f32 v[228:229], v[226:227], v[228:229], s[66:67] op_sel_hi:[1,1,0]
	v_pk_fma_f32 v[234:235], v[232:233], v[234:235], s[66:67] op_sel_hi:[1,1,0]
	v_pk_mul_f32 v[216:217], v[214:215], v[216:217]
	v_pk_mul_f32 v[222:223], v[220:221], v[222:223]
	v_pk_mul_f32 v[228:229], v[226:227], v[228:229]
	v_pk_mul_f32 v[234:235], v[232:233], v[234:235]
	v_pk_mul_f32 v[216:217], v[218:219], v[216:217]
	v_pk_mul_f32 v[222:223], v[224:225], v[222:223]
	v_pk_mul_f32 v[228:229], v[230:231], v[228:229]
	v_pk_mul_f32 v[234:235], v[236:237], v[234:235]
	v_pk_mul_f32 v[214:215], v[8:9], v[216:217]
	v_pk_mul_f32 v[220:221], v[10:11], v[222:223]
	v_pk_mul_f32 v[226:227], v[12:13], v[228:229]
	v_pk_mul_f32 v[232:233], v[14:15], v[234:235]
	v_pk_fma_f32 v[218:219], v[8:9], v[216:217], v[8:9] neg_lo:[1,0,0] neg_hi:[1,0,0]
	v_pk_fma_f32 v[224:225], v[10:11], v[222:223], v[10:11] neg_lo:[1,0,0] neg_hi:[1,0,0]
	v_pk_fma_f32 v[230:231], v[12:13], v[228:229], v[12:13] neg_lo:[1,0,0] neg_hi:[1,0,0]
	v_pk_fma_f32 v[236:237], v[14:15], v[234:235], v[14:15] neg_lo:[1,0,0] neg_hi:[1,0,0]
	v_ashrrev_i32_e32 v216, 31, v8
	v_ashrrev_i32_e32 v217, 31, v9
	v_ashrrev_i32_e32 v222, 31, v10
	v_ashrrev_i32_e32 v223, 31, v11
	v_ashrrev_i32_e32 v228, 31, v12
	v_ashrrev_i32_e32 v229, 31, v13
	v_ashrrev_i32_e32 v234, 31, v14
	v_ashrrev_i32_e32 v235, 31, v15
	v_bfi_b32 v174, v216, v214, v218
	v_bfi_b32 v175, v217, v215, v219
	v_bfi_b32 v179, v222, v220, v224
	v_bfi_b32 v180, v223, v221, v225
	v_bfi_b32 v165, v228, v226, v230
	v_bfi_b32 v167, v229, v227, v231
	v_bfi_b32 v169, v234, v232, v236
	v_bfi_b32 v171, v235, v233, v237
.LBB0_279:
	v_add_u32_e32 v163, 0xb0, v163
	v_mad_i64_i32 v[172:173], s[0:1], v163, s94, v[172:173]
	v_cvt_pk_bf16_f32 v182, v165, v167
	v_cvt_pk_bf16_f32 v183, v169, v171
	v_cvt_pk_bf16_f32 v184, v174, v175
	v_cvt_pk_bf16_f32 v185, v179, v180
	s_and_b64 vcc, exec, s[6:7]
	v_mov_b32_e32 v171, v124
	v_mov_b32_e32 v174, v125
	v_mov_b32_e32 v175, v126
	v_mov_b32_e32 v179, v127
	v_mov_b32_e32 v163, v120
	v_mov_b32_e32 v165, v121
	v_mov_b32_e32 v167, v122
	v_mov_b32_e32 v169, v123
	global_store_dwordx4 v[172:173], v[182:185], off
	s_cbranch_vccnz .LBB0_281
	v_mov_b32_e32 v238, s60
	v_and_b32_e32 v214, 0x7fffffff, v120
	v_and_b32_e32 v215, 0x7fffffff, v121
	v_and_b32_e32 v220, 0x7fffffff, v122
	v_and_b32_e32 v221, 0x7fffffff, v123
	v_and_b32_e32 v226, 0x7fffffff, v124
	v_and_b32_e32 v227, 0x7fffffff, v125
	v_and_b32_e32 v232, 0x7fffffff, v126
	v_and_b32_e32 v233, 0x7fffffff, v127
	v_pk_fma_f32 v[214:215], v[214:215], s[56:57], 1.0 op_sel_hi:[1,0,0]
	v_pk_fma_f32 v[220:221], v[220:221], s[56:57], 1.0 op_sel_hi:[1,0,0]
	v_pk_fma_f32 v[226:227], v[226:227], s[56:57], 1.0 op_sel_hi:[1,0,0]
	v_pk_fma_f32 v[232:233], v[232:233], s[56:57], 1.0 op_sel_hi:[1,0,0]
	v_pk_mul_f32 v[218:219], v[120:121], v[120:121]
	v_pk_mul_f32 v[224:225], v[122:123], v[122:123]
	v_pk_mul_f32 v[230:231], v[124:125], v[124:125]
	v_pk_mul_f32 v[236:237], v[126:127], v[126:127]
	v_rcp_f32_e32 v214, v214
	v_rcp_f32_e32 v215, v215
	v_rcp_f32_e32 v220, v220
	v_rcp_f32_e32 v221, v221
	v_rcp_f32_e32 v226, v226
	v_rcp_f32_e32 v227, v227
	v_rcp_f32_e32 v232, v232
	v_rcp_f32_e32 v233, v233
	v_pk_mul_f32 v[218:219], v[218:219], s[68:69] op_sel_hi:[1,0]
	v_pk_mul_f32 v[224:225], v[224:225], s[68:69] op_sel_hi:[1,0]
	v_pk_mul_f32 v[230:231], v[230:231], s[68:69] op_sel_hi:[1,0]
	v_pk_mul_f32 v[236:237], v[236:237], s[68:69] op_sel_hi:[1,0]
	v_pk_fma_f32 v[216:217], v[214:215], s[58:59], v[238:239] op_sel_hi:[1,0,0]
	v_pk_fma_f32 v[222:223], v[220:221], s[58:59], v[238:239] op_sel_hi:[1,0,0]
	v_pk_fma_f32 v[228:229], v[226:227], s[58:59], v[238:239] op_sel_hi:[1,0,0]
	v_pk_fma_f32 v[234:235], v[232:233], s[58:59], v[238:239] op_sel_hi:[1,0,0]
	v_exp_f32_e32 v218, v218
	v_exp_f32_e32 v219, v219
	v_exp_f32_e32 v224, v224
	v_exp_f32_e32 v225, v225
	v_exp_f32_e32 v230, v230
	v_exp_f32_e32 v231, v231
	v_exp_f32_e32 v236, v236
	v_exp_f32_e32 v237, v237
	v_pk_fma_f32 v[216:217], v[214:215], v[216:217], s[62:63] op_sel_hi:[1,1,0]
	v_pk_fma_f32 v[222:223], v[220:221], v[222:223], s[62:63] op_sel_hi:[1,1,0]
	v_pk_fma_f32 v[228:229], v[226:227], v[228:229], s[62:63] op_sel_hi:[1,1,0]
	v_pk_fma_f32 v[234:235], v[232:233], v[234:235], s[62:63] op_sel_hi:[1,1,0]
	v_pk_fma_f32 v[216:217], v[214:215], v[216:217], s[64:65] op_sel_hi:[1,1,0]
	v_pk_fma_f32 v[222:223], v[220:221], v[222:223], s[64:65] op_sel_hi:[1,1,0]
	v_pk_fma_f32 v[228:229], v[226:227], v[228:229], s[64:65] op_sel_hi:[1,1,0]
	v_pk_fma_f32 v[234:235], v[232:233], v[234:235], s[64:65] op_sel_hi:[1,1,0]
	v_pk_fma_f32 v[216:217], v[214:215], v[216:217], s[66:67] op_sel_hi:[1,1,0]
	v_pk_fma_f32 v[222:223], v[220:221], v[222:223], s[66:67] op_sel_hi:[1,1,0]
	v_pk_fma_f32 v[228:229], v[226:227], v[228:229], s[66:67] op_sel_hi:[1,1,0]
	v_pk_fma_f32 v[234:235], v[232:233], v[234:235], s[66:67] op_sel_hi:[1,1,0]
	v_pk_mul_f32 v[216:217], v[214:215], v[216:217]
	v_pk_mul_f32 v[222:223], v[220:221], v[222:223]
	v_pk_mul_f32 v[228:229], v[226:227], v[228:229]
	v_pk_mul_f32 v[234:235], v[232:233], v[234:235]
	v_pk_mul_f32 v[216:217], v[218:219], v[216:217]
	v_pk_mul_f32 v[222:223], v[224:225], v[222:223]
	v_pk_mul_f32 v[228:229], v[230:231], v[228:229]
	v_pk_mul_f32 v[234:235], v[236:237], v[234:235]
	v_pk_mul_f32 v[214:215], v[120:121], v[216:217]
	v_pk_mul_f32 v[220:221], v[122:123], v[222:223]
	v_pk_mul_f32 v[226:227], v[124:125], v[228:229]
	v_pk_mul_f32 v[232:233], v[126:127], v[234:235]
	v_pk_fma_f32 v[218:219], v[120:121], v[216:217], v[120:121] neg_lo:[1,0,0] neg_hi:[1,0,0]
	v_pk_fma_f32 v[224:225], v[122:123], v[222:223], v[122:123] neg_lo:[1,0,0] neg_hi:[1,0,0]
	v_pk_fma_f32 v[230:231], v[124:125], v[228:229], v[124:125] neg_lo:[1,0,0] neg_hi:[1,0,0]
	v_pk_fma_f32 v[236:237], v[126:127], v[234:235], v[126:127] neg_lo:[1,0,0] neg_hi:[1,0,0]
	v_ashrrev_i32_e32 v216, 31, v120
	v_ashrrev_i32_e32 v217, 31, v121
	v_ashrrev_i32_e32 v222, 31, v122
	v_ashrrev_i32_e32 v223, 31, v123
	v_ashrrev_i32_e32 v228, 31, v124
	v_ashrrev_i32_e32 v229, 31, v125
	v_ashrrev_i32_e32 v234, 31, v126
	v_ashrrev_i32_e32 v235, 31, v127
	v_bfi_b32 v163, v216, v214, v218
	v_bfi_b32 v165, v217, v215, v219
	v_bfi_b32 v167, v222, v220, v224
	v_bfi_b32 v169, v223, v221, v225
	v_bfi_b32 v171, v228, v226, v230
	v_bfi_b32 v174, v229, v227, v231
	v_bfi_b32 v175, v234, v232, v236
	v_bfi_b32 v179, v235, v233, v237
